# row-sum reductions in the norm phases: xor-1/2/4/8 ds_swizzle hops replaced by DPP adds (bit-identical), on top of v040
# speedup vs baseline: 1.0027x; 1.0010x over previous
.LBB0_315:
	v_and_b32_e32 v29, 0xffff0000, v22
	v_and_b32_e32 v31, 0xffff0000, v23
	v_lshlrev_b32_e32 v28, 16, v22
	v_lshlrev_b32_e32 v30, 16, v23
	v_lshlrev_b32_e32 v44, 16, v16
	v_and_b32_e32 v45, 0xffff0000, v16
	v_mul_f32_e32 v2, v29, v29
	v_mul_f32_e32 v16, v31, v31
	v_and_b32_e32 v33, 0xffff0000, v20
	v_and_b32_e32 v35, 0xffff0000, v21
	v_fmac_f32_e32 v2, v28, v28
	v_fmac_f32_e32 v16, v30, v30
	v_lshlrev_b32_e32 v32, 16, v20
	v_lshlrev_b32_e32 v34, 16, v21
	v_lshlrev_b32_e32 v46, 16, v17
	v_and_b32_e32 v47, 0xffff0000, v17
	v_add_f32_e32 v2, v2, v16
	v_mul_f32_e32 v16, v33, v33
	v_mul_f32_e32 v17, v35, v35
	v_fmac_f32_e32 v16, v32, v32
	v_fmac_f32_e32 v17, v34, v34
	v_and_b32_e32 v41, 0xffff0000, v18
	v_and_b32_e32 v43, 0xffff0000, v19
	v_add_f32_e32 v16, v16, v17
	v_lshlrev_b32_e32 v40, 16, v18
	v_lshlrev_b32_e32 v42, 16, v19
	v_add_f32_e32 v2, v2, v16
	v_mul_f32_e32 v16, v41, v41
	v_mul_f32_e32 v17, v43, v43
	v_fmac_f32_e32 v16, v40, v40
	v_fmac_f32_e32 v17, v42, v42
	v_add_f32_e32 v16, v16, v17
	v_add_f32_e32 v2, v16, v2
	v_mul_f32_e32 v16, v45, v45
	v_mul_f32_e32 v17, v47, v47
	v_fmac_f32_e32 v16, v44, v44
	v_fmac_f32_e32 v17, v46, v46
	v_add_f32_e32 v16, v16, v17
	v_add_f32_e32 v2, v16, v2
	s_mul_hi_i32 s6, s15, 0x3e0f83e1
	s_lshr_b32 s17, s6, 31
	s_ashr_i32 s20, s6, 11
	s_waitcnt lgkmcnt(0)
	s_nop 1
	v_add_f32_dpp v2, v2, v2 quad_perm:[1,0,3,2] row_mask:0xf bank_mask:0xf
	s_waitcnt lgkmcnt(0)
	s_nop 1
	v_add_f32_dpp v2, v2, v2 quad_perm:[2,3,0,1] row_mask:0xf bank_mask:0xf
	s_waitcnt lgkmcnt(0)
	s_nop 1
	v_add_f32_dpp v2, v2, v2 row_half_mirror row_mask:0xf bank_mask:0xf
	s_waitcnt lgkmcnt(0)
	s_nop 1
	v_add_f32_dpp v2, v2, v2 row_mirror row_mask:0xf bank_mask:0xf
	ds_swizzle_b32 v16, v2 offset:swizzle(SWAP,16)
	s_waitcnt lgkmcnt(0)
	v_add_f32_e32 v2, v2, v16
	v_mov_b32_e32 v16, v2
	s_nop 1
	v_permlane32_swap_b32_e32 v2, v16
	v_add_f32_e32 v2, v2, v16
	v_fmamk_f32 v2, v2, 0x3a800000, v213
	v_mul_f32_e32 v16, 0x4f800000, v2
	v_cmp_gt_f32_e32 vcc, s3, v2
	s_nop 1
	v_cndmask_b32_e32 v2, v2, v16, vcc
	v_sqrt_f32_e32 v16, v2
	s_nop 0
	v_add_u32_e32 v17, -1, v16
	v_fma_f32 v18, -v17, v16, v2
	v_cmp_ge_f32_e64 s[6:7], 0, v18
	v_add_u32_e32 v18, 1, v16
	s_nop 0
	v_cndmask_b32_e64 v17, v16, v17, s[6:7]
	v_fma_f32 v16, -v18, v16, v2
	v_cmp_lt_f32_e64 s[6:7], 0, v16
	s_nop 1
	v_cndmask_b32_e64 v16, v17, v18, s[6:7]
	v_mul_f32_e32 v17, 0x37800000, v16
	v_cndmask_b32_e32 v16, v16, v17, vcc
	v_cmp_class_f32_e32 vcc, v2, v215
	s_nop 1
	v_cndmask_b32_e32 v2, v16, v2, vcc
	v_div_scale_f32 v16, s[6:7], v2, v2, 1.0
	v_rcp_f32_e32 v17, v16
	s_add_i32 s6, s20, s17
	s_mul_i32 s7, s6, 0xffffdf00
	s_add_i32 s7, s15, s7
	v_fma_f32 v18, -v16, v17, 1.0
	v_fmac_f32_e32 v17, v18, v17
	v_div_scale_f32 v18, vcc, 1.0, v2, 1.0
	v_mul_f32_e32 v19, v18, v17
	v_fma_f32 v20, -v16, v19, v18
	v_fmac_f32_e32 v19, v20, v17
	s_lshl_b32 s6, s6, 13
	v_fma_f32 v16, -v16, v19, v18
	s_cmpk_gt_i32 s7, 0xff
	v_div_fmas_f32 v16, v16, v17, v19
	s_cselect_b32 s6, s6, 0x8000
	v_div_fixup_f32 v2, v16, v2, 1.0
	ds_read_b128 v[16:19], v1
	v_add_u32_e32 v37, s6, v1
	ds_read_b128 v[20:23], v37 offset:8192
	ds_read_b128 v[24:27], v37 offset:4096
	v_pk_mul_f32 v[28:29], v[28:29], v[2:3] op_sel_hi:[1,0]
	v_pk_mul_f32 v[30:31], v[30:31], v[2:3] op_sel_hi:[1,0]
	s_waitcnt lgkmcnt(2)
	v_pk_mul_f32 v[16:17], v[16:17], v[28:29]
	s_waitcnt lgkmcnt(1)
	v_pk_add_f32 v[20:21], v[20:21], 1.0 op_sel_hi:[1,0]
	v_pk_mul_f32 v[18:19], v[18:19], v[30:31]
	v_pk_add_f32 v[22:23], v[22:23], 1.0 op_sel_hi:[1,0]
	s_waitcnt lgkmcnt(0)
	v_pk_fma_f32 v[16:17], v[20:21], v[16:17], v[24:25]
	v_pk_fma_f32 v[18:19], v[22:23], v[18:19], v[26:27]
	v_cvt_pk_bf16_f32 v16, v16, v17
	v_pk_mul_f32 v[30:31], v[32:33], v[2:3] op_sel_hi:[1,0]
	v_cvt_pk_bf16_f32 v17, v18, v19
	global_store_dwordx2 v[6:7], v[16:17], off
	ds_read_b128 v[16:19], v1 offset:1024
	ds_read_b128 v[20:23], v37 offset:9216
	ds_read_b128 v[24:27], v37 offset:5120
	v_pk_mul_f32 v[28:29], v[34:35], v[2:3] op_sel_hi:[1,0]
	s_andn2_b64 vcc, exec, s[34:35]
	s_waitcnt lgkmcnt(2)
	v_pk_mul_f32 v[16:17], v[16:17], v[30:31]
	s_waitcnt lgkmcnt(1)
	v_pk_add_f32 v[20:21], v[20:21], 1.0 op_sel_hi:[1,0]
	v_pk_mul_f32 v[18:19], v[18:19], v[28:29]
	v_pk_add_f32 v[22:23], v[22:23], 1.0 op_sel_hi:[1,0]
	s_waitcnt lgkmcnt(0)
	v_pk_fma_f32 v[16:17], v[20:21], v[16:17], v[24:25]
	v_pk_fma_f32 v[18:19], v[22:23], v[18:19], v[26:27]
	v_cvt_pk_bf16_f32 v16, v16, v17
	v_pk_mul_f32 v[30:31], v[40:41], v[2:3] op_sel_hi:[1,0]
	v_cvt_pk_bf16_f32 v17, v18, v19
	global_store_dwordx2 v[6:7], v[16:17], off offset:512
	ds_read_b128 v[16:19], v1 offset:2048
	ds_read_b128 v[20:23], v37 offset:10240
	ds_read_b128 v[24:27], v37 offset:6144
	v_pk_mul_f32 v[28:29], v[42:43], v[2:3] op_sel_hi:[1,0]
	s_mov_b32 s15, s26
	s_waitcnt lgkmcnt(2)
	v_pk_mul_f32 v[16:17], v[30:31], v[16:17]
	s_waitcnt lgkmcnt(1)
	v_pk_add_f32 v[20:21], v[20:21], 1.0 op_sel_hi:[1,0]
	v_pk_mul_f32 v[18:19], v[28:29], v[18:19]
	v_pk_add_f32 v[22:23], v[22:23], 1.0 op_sel_hi:[1,0]
	s_waitcnt lgkmcnt(0)
	v_pk_fma_f32 v[16:17], v[16:17], v[20:21], v[24:25]
	v_pk_fma_f32 v[18:19], v[18:19], v[22:23], v[26:27]
	v_cvt_pk_bf16_f32 v16, v16, v17
	v_pk_mul_f32 v[30:31], v[44:45], v[2:3] op_sel_hi:[1,0]
	v_cvt_pk_bf16_f32 v17, v18, v19
	global_store_dwordx2 v[6:7], v[16:17], off offset:1024
	ds_read_b128 v[16:19], v1 offset:3072
	ds_read_b128 v[20:23], v37 offset:11264
	ds_read_b128 v[24:27], v37 offset:7168
	v_pk_mul_f32 v[28:29], v[46:47], v[2:3] op_sel_hi:[1,0]
	s_waitcnt lgkmcnt(2)
	v_pk_mul_f32 v[16:17], v[30:31], v[16:17]
	s_waitcnt lgkmcnt(1)
	v_pk_add_f32 v[20:21], v[20:21], 1.0 op_sel_hi:[1,0]
	v_pk_mul_f32 v[18:19], v[28:29], v[18:19]
	v_pk_add_f32 v[22:23], v[22:23], 1.0 op_sel_hi:[1,0]
	s_waitcnt lgkmcnt(0)
	v_pk_fma_f32 v[16:17], v[16:17], v[20:21], v[24:25]
	v_pk_fma_f32 v[18:19], v[18:19], v[22:23], v[26:27]
	v_cvt_pk_bf16_f32 v16, v16, v17
	s_waitcnt vmcnt(6)
	v_mov_b32_e32 v22, v8
	v_cvt_pk_bf16_f32 v17, v18, v19
	global_store_dwordx2 v[6:7], v[16:17], off offset:1536
	v_lshl_add_u64 v[6:7], v[6:7], 0, s[24:25]
	v_mov_b32_e32 v23, v9
	s_waitcnt vmcnt(6)
	v_mov_b32_e32 v20, v10
	v_mov_b32_e32 v21, v11
	s_waitcnt vmcnt(5)
	v_mov_b32_e32 v18, v12
	v_mov_b32_e32 v19, v13
	s_waitcnt vmcnt(4)
	v_mov_b32_e32 v16, v14
	v_mov_b32_e32 v17, v15
	s_cbranch_vccz .LBB0_319

.LBB0_356:
	s_mul_hi_i32 s7, s6, 0x3e0f83e1
	s_lshr_b32 s15, s7, 31
	s_ashr_i32 s7, s7, 11
	s_add_i32 s7, s7, s15
	s_mul_i32 s15, s7, 0xffffdf00
	s_add_i32 s6, s6, s15
	s_cmpk_gt_i32 s6, 0xff
	s_cselect_b32 s15, s7, 4
	v_lshl_add_u32 v2, s15, 12, v1
	v_lshlrev_b32_e32 v62, 16, v26
	v_and_b32_e32 v63, 0xffff0000, v26
	v_lshlrev_b32_e32 v64, 16, v27
	v_and_b32_e32 v65, 0xffff0000, v27
	v_lshlrev_b32_e32 v66, 16, v24
	v_and_b32_e32 v67, 0xffff0000, v24
	v_lshlrev_b32_e32 v68, 16, v25
	v_and_b32_e32 v69, 0xffff0000, v25
	ds_read_b128 v[24:27], v2 offset:45056
	v_lshlrev_b32_e32 v58, 16, v30
	v_and_b32_e32 v59, 0xffff0000, v30
	v_lshlrev_b32_e32 v60, 16, v31
	v_and_b32_e32 v61, 0xffff0000, v31
	s_waitcnt vmcnt(3)
	v_lshlrev_b32_e32 v31, 16, v50
	v_lshlrev_b32_e32 v30, 16, v48
	v_and_b32_e32 v53, 0xffff0000, v50
	v_and_b32_e32 v52, 0xffff0000, v48
	v_pk_mul_f32 v[30:31], v[22:23], v[30:31]
	v_pk_mul_f32 v[52:53], v[22:23], v[52:53]
	v_mov_b32_e32 v54, v30
	v_mov_b32_e32 v55, v52
	v_mov_b32_e32 v52, v31
	v_lshlrev_b32_e32 v56, 16, v46
	v_and_b32_e32 v57, 0xffff0000, v46
	v_pk_add_f32 v[30:31], v[54:55], v[52:53]
	ds_read_b128 v[52:55], v2 offset:46080
	s_waitcnt lgkmcnt(1)
	v_pk_fma_f32 v[24:25], v[30:31], v[24:25], v[56:57]
	v_lshlrev_b32_e32 v31, 16, v51
	v_lshlrev_b32_e32 v30, 16, v49
	v_and_b32_e32 v51, 0xffff0000, v51
	v_and_b32_e32 v50, 0xffff0000, v49
	v_pk_mul_f32 v[30:31], v[22:23], v[30:31]
	v_pk_mul_f32 v[48:49], v[22:23], v[50:51]
	v_mov_b32_e32 v50, v30
	v_mov_b32_e32 v51, v48
	v_mov_b32_e32 v48, v31
	v_lshlrev_b32_e32 v46, 16, v47
	v_and_b32_e32 v47, 0xffff0000, v47
	v_pk_add_f32 v[30:31], v[50:51], v[48:49]
	s_mov_b32 s6, 0xf7c00000
	v_pk_fma_f32 v[30:31], v[30:31], v[26:27], v[46:47]
	s_waitcnt vmcnt(2)
	v_lshlrev_b32_e32 v27, 16, v44
	v_lshlrev_b32_e32 v26, 16, v42
	v_and_b32_e32 v47, 0xffff0000, v44
	v_and_b32_e32 v46, 0xffff0000, v42
	v_pk_mul_f32 v[26:27], v[22:23], v[26:27]
	v_pk_mul_f32 v[46:47], v[22:23], v[46:47]
	v_mov_b32_e32 v48, v26
	v_mov_b32_e32 v49, v46
	v_mov_b32_e32 v46, v27
	v_pk_add_f32 v[26:27], v[48:49], v[46:47]
	v_lshlrev_b32_e32 v47, 16, v45
	v_lshlrev_b32_e32 v46, 16, v43
	v_and_b32_e32 v45, 0xffff0000, v45
	v_and_b32_e32 v44, 0xffff0000, v43
	v_pk_mul_f32 v[46:47], v[22:23], v[46:47]
	v_pk_mul_f32 v[42:43], v[22:23], v[44:45]
	v_mov_b32_e32 v44, v46
	v_mov_b32_e32 v45, v42
	v_mov_b32_e32 v42, v47
	v_pk_add_f32 v[42:43], v[44:45], v[42:43]
	s_waitcnt vmcnt(1)
	v_lshlrev_b32_e32 v47, 16, v40
	s_waitcnt lgkmcnt(0)
	v_pk_fma_f32 v[50:51], v[42:43], v[54:55], v[60:61]
	ds_read_b128 v[42:45], v2 offset:47104
	v_lshlrev_b32_e32 v46, 16, v34
	v_and_b32_e32 v49, 0xffff0000, v40
	v_and_b32_e32 v48, 0xffff0000, v34
	v_pk_mul_f32 v[46:47], v[22:23], v[46:47]
	v_pk_mul_f32 v[48:49], v[22:23], v[48:49]
	v_pk_fma_f32 v[26:27], v[26:27], v[52:53], v[58:59]
	v_mov_b32_e32 v52, v46
	v_mov_b32_e32 v53, v48
	v_mov_b32_e32 v48, v47
	v_pk_add_f32 v[52:53], v[52:53], v[48:49]
	ds_read_b128 v[46:49], v2 offset:48128
	s_waitcnt lgkmcnt(1)
	v_pk_fma_f32 v[52:53], v[52:53], v[42:43], v[62:63]
	v_lshlrev_b32_e32 v43, 16, v41
	v_lshlrev_b32_e32 v42, 16, v35
	v_and_b32_e32 v41, 0xffff0000, v41
	v_and_b32_e32 v40, 0xffff0000, v35
	v_pk_mul_f32 v[42:43], v[22:23], v[42:43]
	v_pk_mul_f32 v[34:35], v[22:23], v[40:41]
	v_mov_b32_e32 v40, v42
	v_mov_b32_e32 v41, v34
	v_mov_b32_e32 v34, v43
	v_pk_add_f32 v[34:35], v[40:41], v[34:35]
	s_waitcnt vmcnt(0)
	v_and_b32_e32 v41, 0xffff0000, v32
	v_pk_fma_f32 v[54:55], v[34:35], v[44:45], v[64:65]
	v_lshlrev_b32_e32 v35, 16, v32
	v_lshlrev_b32_e32 v34, 16, v28
	v_and_b32_e32 v40, 0xffff0000, v28
	v_pk_mul_f32 v[34:35], v[22:23], v[34:35]
	v_pk_mul_f32 v[40:41], v[22:23], v[40:41]
	v_mov_b32_e32 v42, v34
	v_mov_b32_e32 v43, v40
	v_mov_b32_e32 v40, v35
	v_pk_add_f32 v[34:35], v[42:43], v[40:41]
	v_and_b32_e32 v32, 0xffff0000, v29
	s_waitcnt lgkmcnt(0)
	v_pk_fma_f32 v[56:57], v[34:35], v[46:47], v[66:67]
	v_lshlrev_b32_e32 v35, 16, v33
	v_lshlrev_b32_e32 v34, 16, v29
	v_and_b32_e32 v33, 0xffff0000, v33
	v_pk_mul_f32 v[34:35], v[22:23], v[34:35]
	v_pk_mul_f32 v[22:23], v[22:23], v[32:33]
	v_mov_b32_e32 v28, v34
	v_mov_b32_e32 v29, v22
	v_mov_b32_e32 v22, v35
	v_pk_add_f32 v[22:23], v[28:29], v[22:23]
	v_pk_mul_f32 v[28:29], v[30:31], v[30:31]
	v_pk_fma_f32 v[48:49], v[22:23], v[48:49], v[68:69]
	v_pk_mul_f32 v[22:23], v[24:25], v[24:25]
	v_pk_mul_f32 v[32:33], v[26:27], v[26:27]
	v_pk_mul_f32 v[34:35], v[50:51], v[50:51]
	v_add_f32_e32 v32, v32, v33
	v_add_f32_e32 v2, v34, v35
	v_add_f32_e32 v28, v28, v29
	v_add_f32_e32 v22, v22, v23
	v_pk_mul_f32 v[40:41], v[52:53], v[52:53]
	v_pk_mul_f32 v[42:43], v[54:55], v[54:55]
	v_add_f32_e32 v2, v32, v2
	v_add_f32_e32 v22, v22, v28
	v_add_f32_e32 v2, v22, v2
	v_add_f32_e32 v22, v42, v43
	v_add_f32_e32 v23, v40, v41
	v_pk_mul_f32 v[44:45], v[56:57], v[56:57]
	v_pk_mul_f32 v[46:47], v[48:49], v[48:49]
	v_add_f32_e32 v22, v23, v22
	v_add_f32_e32 v2, v2, v22
	v_add_f32_e32 v22, v46, v47
	v_add_f32_e32 v23, v44, v45
	v_add_f32_e32 v22, v23, v22
	v_add_f32_e32 v2, v2, v22
	v_lshl_add_u32 v37, s15, 13, v1
	s_waitcnt lgkmcnt(0)
	s_nop 1
	v_add_f32_dpp v2, v2, v2 quad_perm:[1,0,3,2] row_mask:0xf bank_mask:0xf
	s_waitcnt lgkmcnt(0)
	s_nop 1
	v_add_f32_dpp v2, v2, v2 quad_perm:[2,3,0,1] row_mask:0xf bank_mask:0xf
	v_cvt_pk_bf16_f32 v22, v24, v25
	v_cvt_pk_bf16_f32 v23, v30, v31
	s_waitcnt lgkmcnt(0)
	s_nop 1
	v_add_f32_dpp v2, v2, v2 row_half_mirror row_mask:0xf bank_mask:0xf
	v_add_co_u32_e32 v28, vcc, s6, v10
	s_waitcnt lgkmcnt(0)
	s_nop 1
	v_add_f32_dpp v2, v2, v2 row_mirror row_mask:0xf bank_mask:0xf
	ds_swizzle_b32 v32, v2 offset:swizzle(SWAP,16)
	v_addc_co_u32_e32 v29, vcc, -1, v11, vcc
	global_store_dwordx2 v[28:29], v[22:23], off offset:-1536
	v_cvt_pk_bf16_f32 v22, v26, v27
	s_waitcnt lgkmcnt(0)
	v_add_f32_e32 v2, v2, v32
	v_cvt_pk_bf16_f32 v23, v50, v51
	global_store_dwordx2 v[28:29], v[22:23], off offset:-1024
	v_mov_b32_e32 v22, v2
	s_nop 1
	v_permlane32_swap_b32_e32 v2, v22
	v_add_f32_e32 v2, v2, v22
	v_fmamk_f32 v2, v2, 0x3a800000, v213
	v_mul_f32_e32 v22, 0x4f800000, v2
	v_cmp_gt_f32_e32 vcc, s3, v2
	s_nop 1
	v_cndmask_b32_e32 v2, v2, v22, vcc
	v_sqrt_f32_e32 v32, v2
	v_cvt_pk_bf16_f32 v22, v52, v53
	v_cvt_pk_bf16_f32 v23, v54, v55
	global_store_dwordx2 v[28:29], v[22:23], off offset:-512
	v_add_u32_e32 v22, -1, v32
	v_fma_f32 v23, -v22, v32, v2
	v_cmp_ge_f32_e64 s[6:7], 0, v23
	v_add_u32_e32 v23, 1, v32
	s_nop 0
	v_cndmask_b32_e64 v22, v32, v22, s[6:7]
	v_fma_f32 v32, -v23, v32, v2
	v_cmp_lt_f32_e64 s[6:7], 0, v32
	s_nop 1
	v_cndmask_b32_e64 v22, v22, v23, s[6:7]
	v_mul_f32_e32 v23, 0x37800000, v22
	v_cndmask_b32_e32 v22, v22, v23, vcc
	v_cmp_class_f32_e32 vcc, v2, v215
	s_nop 1
	v_cndmask_b32_e32 v2, v22, v2, vcc
	v_div_scale_f32 v32, s[6:7], v2, v2, 1.0
	v_rcp_f32_e32 v33, v32
	v_cvt_pk_bf16_f32 v22, v56, v57
	v_cvt_pk_bf16_f32 v23, v48, v49
	global_store_dwordx2 v[28:29], v[22:23], off
	v_fma_f32 v22, -v32, v33, 1.0
	v_fmac_f32_e32 v33, v22, v33
	v_div_scale_f32 v22, vcc, 1.0, v2, 1.0
	v_mul_f32_e32 v23, v22, v33
	v_fma_f32 v28, -v32, v23, v22
	v_fmac_f32_e32 v23, v28, v33
	v_fma_f32 v22, -v32, v23, v22
	v_div_fmas_f32 v22, v22, v33, v23
	ds_read_b128 v[32:35], v1
	ds_read_b128 v[40:43], v37 offset:8192
	ds_read_b128 v[44:47], v37 offset:4096
	v_div_fixup_f32 v2, v22, v2, 1.0
	v_pk_mul_f32 v[24:25], v[24:25], v[2:3] op_sel_hi:[1,0]
	v_pk_mul_f32 v[22:23], v[30:31], v[2:3] op_sel_hi:[1,0]
	s_waitcnt lgkmcnt(2)
	v_pk_mul_f32 v[24:25], v[32:33], v[24:25]
	s_waitcnt lgkmcnt(1)
	v_pk_add_f32 v[30:31], v[40:41], 1.0 op_sel_hi:[1,0]
	v_pk_mul_f32 v[22:23], v[34:35], v[22:23]
	v_pk_add_f32 v[28:29], v[42:43], 1.0 op_sel_hi:[1,0]
	s_waitcnt lgkmcnt(0)
	v_pk_fma_f32 v[24:25], v[30:31], v[24:25], v[44:45]
	v_pk_fma_f32 v[22:23], v[28:29], v[22:23], v[46:47]
	v_cvt_pk_bf16_f32 v24, v24, v25
	v_pk_mul_f32 v[26:27], v[26:27], v[2:3] op_sel_hi:[1,0]
	v_cvt_pk_bf16_f32 v25, v22, v23
	global_store_dwordx2 v[10:11], v[24:25], off offset:-1536
	ds_read_b128 v[22:25], v1 offset:1024
	ds_read_b128 v[28:31], v37 offset:9216
	ds_read_b128 v[32:35], v37 offset:5120
	v_pk_mul_f32 v[40:41], v[50:51], v[2:3] op_sel_hi:[1,0]
	s_and_b64 vcc, exec, s[26:27]
	s_waitcnt lgkmcnt(2)
	v_pk_mul_f32 v[22:23], v[22:23], v[26:27]
	s_waitcnt lgkmcnt(1)
	v_pk_add_f32 v[28:29], v[28:29], 1.0 op_sel_hi:[1,0]
	v_pk_mul_f32 v[24:25], v[24:25], v[40:41]
	v_pk_add_f32 v[26:27], v[30:31], 1.0 op_sel_hi:[1,0]
	s_waitcnt lgkmcnt(0)
	v_pk_fma_f32 v[22:23], v[28:29], v[22:23], v[32:33]
	v_pk_fma_f32 v[24:25], v[26:27], v[24:25], v[34:35]
	v_cvt_pk_bf16_f32 v22, v22, v23
	v_pk_mul_f32 v[40:41], v[52:53], v[2:3] op_sel_hi:[1,0]
	v_cvt_pk_bf16_f32 v23, v24, v25
	global_store_dwordx2 v[10:11], v[22:23], off offset:-1024
	ds_read_b128 v[22:25], v1 offset:2048
	ds_read_b128 v[26:29], v37 offset:10240
	ds_read_b128 v[30:33], v37 offset:6144
	v_pk_mul_f32 v[34:35], v[54:55], v[2:3] op_sel_hi:[1,0]
	v_mov_b64_e32 v[46:47], v[18:19]
	s_waitcnt lgkmcnt(2)
	v_pk_mul_f32 v[22:23], v[40:41], v[22:23]
	s_waitcnt lgkmcnt(1)
	v_pk_add_f32 v[26:27], v[26:27], 1.0 op_sel_hi:[1,0]
	v_pk_mul_f32 v[24:25], v[34:35], v[24:25]
	v_pk_add_f32 v[28:29], v[28:29], 1.0 op_sel_hi:[1,0]
	s_waitcnt lgkmcnt(0)
	v_pk_fma_f32 v[22:23], v[22:23], v[26:27], v[30:31]
	v_pk_fma_f32 v[24:25], v[24:25], v[28:29], v[32:33]
	v_cvt_pk_bf16_f32 v22, v22, v23
	v_pk_mul_f32 v[40:41], v[56:57], v[2:3] op_sel_hi:[1,0]
	v_cvt_pk_bf16_f32 v23, v24, v25
	global_store_dwordx2 v[10:11], v[22:23], off offset:-512
	ds_read_b128 v[22:25], v1 offset:3072
	ds_read_b128 v[26:29], v37 offset:11264
	ds_read_b128 v[30:33], v37 offset:7168
	v_pk_mul_f32 v[34:35], v[48:49], v[2:3] op_sel_hi:[1,0]
	s_mov_b32 s6, s24
	s_waitcnt lgkmcnt(2)
	v_pk_mul_f32 v[22:23], v[40:41], v[22:23]
	s_waitcnt lgkmcnt(1)
	v_pk_add_f32 v[26:27], v[26:27], 1.0 op_sel_hi:[1,0]
	v_pk_mul_f32 v[24:25], v[34:35], v[24:25]
	v_pk_add_f32 v[28:29], v[28:29], 1.0 op_sel_hi:[1,0]
	s_waitcnt lgkmcnt(0)
	v_pk_fma_f32 v[22:23], v[22:23], v[26:27], v[30:31]
	v_pk_fma_f32 v[24:25], v[24:25], v[28:29], v[32:33]
	v_cvt_pk_bf16_f32 v22, v22, v23
	v_mov_b64_e32 v[26:27], v[14:15]
	v_cvt_pk_bf16_f32 v23, v24, v25
	global_store_dwordx2 v[10:11], v[22:23], off
	v_lshl_add_u64 v[10:11], v[10:11], 0, s[10:11]
	v_mov_b64_e32 v[24:25], v[12:13]
	v_mov_b64_e32 v[30:31], v[16:17]
	v_mov_b64_e32 v[22:23], v[20:21]
	s_cbranch_vccnz .LBB0_359

.LBB0_376:
	v_mul_f32_e32 v37, v17, v17
	v_mul_f32_e32 v39, v19, v19
	v_fmac_f32_e32 v37, v16, v16
	v_fmac_f32_e32 v39, v18, v18
	v_add_f32_e32 v37, v37, v39
	v_mul_f32_e32 v39, v13, v13
	v_mul_f32_e32 v42, v15, v15
	v_fmac_f32_e32 v39, v12, v12
	v_fmac_f32_e32 v42, v14, v14
	v_add_f32_e32 v39, v39, v42
	v_add_f32_e32 v37, v37, v39
	v_mul_f32_e32 v39, v9, v9
	v_mul_f32_e32 v42, v11, v11
	v_fmac_f32_e32 v39, v8, v8
	v_fmac_f32_e32 v42, v10, v10
	v_add_f32_e32 v39, v39, v42
	v_add_f32_e32 v37, v39, v37
	v_mul_f32_e32 v39, v5, v5
	v_mul_f32_e32 v42, v7, v7
	v_fmac_f32_e32 v39, v4, v4
	v_fmac_f32_e32 v42, v6, v6
	v_add_f32_e32 v39, v39, v42
	v_add_f32_e32 v37, v39, v37
	v_add_co_u32_e32 v44, vcc, s40, v40
	v_cvt_pk_bf16_f32 v42, v16, v17
	s_mul_hi_i32 s5, s4, 0x3e0f83e1
	s_waitcnt lgkmcnt(0)
	s_nop 1
	v_add_f32_dpp v37, v37, v37 quad_perm:[1,0,3,2] row_mask:0xf bank_mask:0xf
	v_addc_co_u32_e32 v45, vcc, -1, v41, vcc
	v_cvt_pk_bf16_f32 v43, v18, v19
	global_store_dwordx2 v[44:45], v[42:43], off offset:-1536
	s_waitcnt lgkmcnt(0)
	s_nop 1
	v_add_f32_dpp v37, v37, v37 quad_perm:[2,3,0,1] row_mask:0xf bank_mask:0xf
	v_cvt_pk_bf16_f32 v42, v12, v13
	s_lshr_b32 s17, s5, 31
	s_ashr_i32 s5, s5, 11
	v_cvt_pk_bf16_f32 v43, v14, v15
	s_waitcnt lgkmcnt(0)
	s_nop 1
	v_add_f32_dpp v37, v37, v37 row_half_mirror row_mask:0xf bank_mask:0xf
	global_store_dwordx2 v[44:45], v[42:43], off offset:-1024
	v_cvt_pk_bf16_f32 v42, v8, v9
	s_add_i32 s17, s5, s17
	v_cvt_pk_bf16_f32 v43, v10, v11
	s_waitcnt lgkmcnt(0)
	s_nop 1
	v_add_f32_dpp v37, v37, v37 row_mirror row_mask:0xf bank_mask:0xf
	ds_swizzle_b32 v39, v37 offset:swizzle(SWAP,16)
	global_store_dwordx2 v[44:45], v[42:43], off offset:-512
	s_mul_i32 s5, s17, 0xffffdf00
	s_add_i32 s20, s4, s5
	s_waitcnt lgkmcnt(0)
	v_add_f32_e32 v37, v37, v39
	v_mov_b32_e32 v39, v37
	s_nop 1
	v_permlane32_swap_b32_e32 v37, v39
	v_add_f32_e32 v37, v37, v39
	v_fmamk_f32 v37, v37, 0x3a800000, v213
	v_mul_f32_e32 v39, 0x4f800000, v37
	v_cmp_gt_f32_e32 vcc, s3, v37
	s_nop 1
	v_cndmask_b32_e32 v37, v37, v39, vcc
	v_sqrt_f32_e32 v39, v37
	s_nop 0
	v_add_u32_e32 v42, -1, v39
	v_fma_f32 v43, -v42, v39, v37
	v_cmp_ge_f32_e64 s[4:5], 0, v43
	v_add_u32_e32 v43, 1, v39
	s_nop 0
	v_cndmask_b32_e64 v42, v39, v42, s[4:5]
	v_fma_f32 v39, -v43, v39, v37
	v_cmp_lt_f32_e64 s[4:5], 0, v39
	s_nop 1
	v_cndmask_b32_e64 v39, v42, v43, s[4:5]
	v_mul_f32_e32 v42, 0x37800000, v39
	v_cndmask_b32_e32 v39, v39, v42, vcc
	v_cmp_class_f32_e32 vcc, v37, v215
	v_cvt_pk_bf16_f32 v42, v4, v5
	v_cvt_pk_bf16_f32 v43, v6, v7
	global_store_dwordx2 v[44:45], v[42:43], off
	s_nop 0
	v_cndmask_b32_e32 v37, v39, v37, vcc
	v_div_scale_f32 v39, s[4:5], v37, v37, 1.0
	v_rcp_f32_e32 v46, v39
	s_lshl_b32 s4, s17, 13
	s_cmpk_gt_i32 s20, 0xff
	s_cselect_b32 s4, s4, 0x8000
	v_fma_f32 v42, -v39, v46, 1.0
	v_fmac_f32_e32 v46, v42, v46
	v_div_scale_f32 v42, vcc, 1.0, v37, 1.0
	v_mul_f32_e32 v43, v42, v46
	v_fma_f32 v44, -v39, v43, v42
	v_fmac_f32_e32 v43, v44, v46
	v_fma_f32 v39, -v39, v43, v42
	v_div_fmas_f32 v39, v39, v46, v43
	v_div_fixup_f32 v54, v39, v37, 1.0
	ds_read_b128 v[42:45], v1
	v_add_u32_e32 v37, s4, v1
	ds_read_b128 v[46:49], v37 offset:8192
	ds_read_b128 v[50:53], v37 offset:4096
	v_pk_mul_f32 v[18:19], v[18:19], v[54:55] op_sel_hi:[1,0]
	v_pk_mul_f32 v[16:17], v[16:17], v[54:55] op_sel_hi:[1,0]
	s_waitcnt lgkmcnt(2)
	v_pk_mul_f32 v[18:19], v[44:45], v[18:19]
	v_pk_mul_f32 v[16:17], v[42:43], v[16:17]
	s_waitcnt lgkmcnt(1)
	v_pk_add_f32 v[44:45], v[46:47], 1.0 op_sel_hi:[1,0]
	v_pk_add_f32 v[42:43], v[48:49], 1.0 op_sel_hi:[1,0]
	s_waitcnt lgkmcnt(0)
	v_pk_fma_f32 v[16:17], v[44:45], v[16:17], v[50:51]
	v_pk_fma_f32 v[18:19], v[42:43], v[18:19], v[52:53]
	v_cvt_pk_bf16_f32 v16, v16, v17
	v_pk_mul_f32 v[14:15], v[14:15], v[54:55] op_sel_hi:[1,0]
	v_cvt_pk_bf16_f32 v17, v18, v19
	global_store_dwordx2 v[40:41], v[16:17], off offset:-1536
	ds_read_b128 v[16:19], v1 offset:1024
	ds_read_b128 v[42:45], v37 offset:9216
	ds_read_b128 v[46:49], v37 offset:5120
	v_pk_mul_f32 v[12:13], v[12:13], v[54:55] op_sel_hi:[1,0]
	v_pk_mul_f32 v[10:11], v[10:11], v[54:55] op_sel_hi:[1,0]
	s_waitcnt lgkmcnt(2)
	v_pk_mul_f32 v[12:13], v[16:17], v[12:13]
	v_pk_mul_f32 v[14:15], v[18:19], v[14:15]
	s_waitcnt lgkmcnt(1)
	v_pk_add_f32 v[18:19], v[42:43], 1.0 op_sel_hi:[1,0]
	v_pk_add_f32 v[16:17], v[44:45], 1.0 op_sel_hi:[1,0]
	s_waitcnt lgkmcnt(0)
	v_pk_fma_f32 v[12:13], v[18:19], v[12:13], v[46:47]
	v_pk_fma_f32 v[14:15], v[16:17], v[14:15], v[48:49]
	v_cvt_pk_bf16_f32 v12, v12, v13
	v_pk_mul_f32 v[8:9], v[8:9], v[54:55] op_sel_hi:[1,0]
	v_cvt_pk_bf16_f32 v13, v14, v15
	global_store_dwordx2 v[40:41], v[12:13], off offset:-1024
	ds_read_b128 v[12:15], v1 offset:2048
	ds_read_b128 v[16:19], v37 offset:10240
	ds_read_b128 v[42:45], v37 offset:6144
	v_pk_mul_f32 v[6:7], v[6:7], v[54:55] op_sel_hi:[1,0]
	v_pk_mul_f32 v[4:5], v[4:5], v[54:55] op_sel_hi:[1,0]
	s_waitcnt lgkmcnt(2)
	v_pk_mul_f32 v[8:9], v[8:9], v[12:13]
	v_pk_mul_f32 v[10:11], v[10:11], v[14:15]
	s_waitcnt lgkmcnt(1)
	v_pk_add_f32 v[14:15], v[16:17], 1.0 op_sel_hi:[1,0]
	v_pk_add_f32 v[12:13], v[18:19], 1.0 op_sel_hi:[1,0]
	s_waitcnt lgkmcnt(0)
	v_pk_fma_f32 v[8:9], v[8:9], v[14:15], v[42:43]
	v_pk_fma_f32 v[10:11], v[10:11], v[12:13], v[44:45]
	v_cvt_pk_bf16_f32 v8, v8, v9
	s_and_b64 vcc, exec, s[24:25]
	v_cvt_pk_bf16_f32 v9, v10, v11
	global_store_dwordx2 v[40:41], v[8:9], off offset:-512
	ds_read_b128 v[8:11], v1 offset:3072
	ds_read_b128 v[12:15], v37 offset:11264
	ds_read_b128 v[16:19], v37 offset:7168
	s_mov_b32 s4, s15
	s_waitcnt lgkmcnt(2)
	v_pk_mul_f32 v[4:5], v[4:5], v[8:9]
	v_pk_mul_f32 v[6:7], v[6:7], v[10:11]
	s_waitcnt lgkmcnt(1)
	v_pk_add_f32 v[10:11], v[12:13], 1.0 op_sel_hi:[1,0]
	v_pk_add_f32 v[8:9], v[14:15], 1.0 op_sel_hi:[1,0]
	s_waitcnt lgkmcnt(0)
	v_pk_fma_f32 v[4:5], v[4:5], v[10:11], v[16:17]
	v_pk_fma_f32 v[6:7], v[6:7], v[8:9], v[18:19]
	v_cvt_pk_bf16_f32 v4, v4, v5
	s_waitcnt vmcnt(10)
	v_mov_b32_e32 v16, v20
	v_cvt_pk_bf16_f32 v5, v6, v7
	global_store_dwordx2 v[40:41], v[4:5], off
	v_lshl_add_u64 v[40:41], v[40:41], 0, s[8:9]
	v_mov_b32_e32 v17, v21
	v_mov_b32_e32 v18, v22
	v_mov_b32_e32 v19, v23
	s_waitcnt vmcnt(10)
	v_mov_b32_e32 v12, v24
	v_mov_b32_e32 v13, v25
	v_mov_b32_e32 v14, v26
	v_mov_b32_e32 v15, v27
	s_waitcnt vmcnt(9)
	v_mov_b32_e32 v8, v28
	v_mov_b32_e32 v9, v29
	v_mov_b32_e32 v10, v30
	v_mov_b32_e32 v11, v31
	s_waitcnt vmcnt(8)
	v_mov_b32_e32 v4, v32
	v_mov_b32_e32 v5, v33
	v_mov_b32_e32 v6, v34
	v_mov_b32_e32 v7, v35
	s_cbranch_vccnz .LBB0_379

.LBB0_1289:
	s_waitcnt vmcnt(12)
	v_and_b32_e32 v197, 0xffff0000, v184
	v_and_b32_e32 v217, 0xffff0000, v185
	v_lshlrev_b32_e32 v196, 16, v184
	v_lshlrev_b32_e32 v216, 16, v185
	v_mul_f32_e32 v2, v197, v197
	v_mul_f32_e32 v133, v217, v217
	v_fmac_f32_e32 v2, v196, v196
	v_fmac_f32_e32 v133, v216, v216
	v_and_b32_e32 v199, 0xffff0000, v182
	v_and_b32_e32 v201, 0xffff0000, v183
	v_add_f32_e32 v2, v2, v133
	v_lshlrev_b32_e32 v198, 16, v182
	v_lshlrev_b32_e32 v200, 16, v183
	v_mul_f32_e32 v133, v199, v199
	v_mul_f32_e32 v182, v201, v201
	v_fmac_f32_e32 v133, v198, v198
	v_fmac_f32_e32 v182, v200, v200
	v_add_f32_e32 v133, v133, v182
	v_and_b32_e32 v193, 0xffff0000, v178
	v_and_b32_e32 v195, 0xffff0000, v179
	v_add_f32_e32 v2, v2, v133
	v_lshlrev_b32_e32 v192, 16, v178
	v_lshlrev_b32_e32 v194, 16, v179
	v_mul_f32_e32 v133, v193, v193
	v_mul_f32_e32 v178, v195, v195
	v_fmac_f32_e32 v133, v192, v192
	v_fmac_f32_e32 v178, v194, v194
	v_add_f32_e32 v133, v133, v178
	v_lshlrev_b32_e32 v178, 16, v180
	v_and_b32_e32 v179, 0xffff0000, v180
	v_lshlrev_b32_e32 v180, 16, v181
	v_and_b32_e32 v181, 0xffff0000, v181
	v_add_f32_e32 v2, v2, v133
	v_mul_f32_e32 v133, v179, v179
	v_mul_f32_e32 v182, v181, v181
	v_fmac_f32_e32 v133, v178, v178
	v_fmac_f32_e32 v182, v180, v180
	v_add_f32_e32 v133, v133, v182
	v_add_f32_e32 v2, v2, v133
	s_lshl_b32 s16, s16, 13
	s_waitcnt lgkmcnt(0)
	s_nop 1
	v_add_f32_dpp v2, v2, v2 quad_perm:[1,0,3,2] row_mask:0xf bank_mask:0xf
	s_waitcnt lgkmcnt(0)
	s_nop 1
	v_add_f32_dpp v2, v2, v2 quad_perm:[2,3,0,1] row_mask:0xf bank_mask:0xf
	s_waitcnt lgkmcnt(0)
	s_nop 1
	v_add_f32_dpp v2, v2, v2 row_half_mirror row_mask:0xf bank_mask:0xf
	s_waitcnt lgkmcnt(0)
	s_nop 1
	v_add_f32_dpp v2, v2, v2 row_mirror row_mask:0xf bank_mask:0xf
	ds_swizzle_b32 v133, v2 offset:swizzle(SWAP,16)
	s_waitcnt lgkmcnt(0)
	v_add_f32_e32 v2, v2, v133
	v_mov_b32_e32 v133, v2
	s_nop 1
	v_permlane32_swap_b32_e32 v2, v133
	v_add_f32_e32 v2, v2, v133
	v_fmamk_f32 v2, v2, 0x3a800000, v213
	v_mul_f32_e32 v133, 0x4f800000, v2
	v_cmp_gt_f32_e32 vcc, s3, v2
	s_nop 1
	v_cndmask_b32_e32 v2, v2, v133, vcc
	v_sqrt_f32_e32 v133, v2
	s_nop 0
	v_add_u32_e32 v182, -1, v133
	v_fma_f32 v183, -v182, v133, v2
	v_cmp_ge_f32_e64 s[12:13], 0, v183
	v_add_u32_e32 v183, 1, v133
	s_nop 0
	v_cndmask_b32_e64 v182, v133, v182, s[12:13]
	v_fma_f32 v133, -v183, v133, v2
	v_cmp_lt_f32_e64 s[12:13], 0, v133
	s_nop 1
	v_cndmask_b32_e64 v133, v182, v183, s[12:13]
	v_mul_f32_e32 v182, 0x37800000, v133
	v_cndmask_b32_e32 v133, v133, v182, vcc
	v_cmp_class_f32_e32 vcc, v2, v215
	s_and_b64 s[12:13], s[14:15], exec
	s_cselect_b32 s14, 0x8000, s16
	v_cndmask_b32_e32 v2, v133, v2, vcc
	v_div_scale_f32 v133, s[12:13], v2, v2, 1.0
	v_rcp_f32_e32 v182, v133
	s_ashr_i32 s35, s34, 31
	s_lshl_b64 s[12:13], s[34:35], 11
	v_fma_f32 v183, -v133, v182, 1.0
	v_fmac_f32_e32 v182, v183, v182
	v_div_scale_f32 v183, vcc, 1.0, v2, 1.0
	v_mul_f32_e32 v184, v183, v182
	v_fma_f32 v185, -v133, v184, v183
	v_fmac_f32_e32 v184, v185, v182
	v_fma_f32 v133, -v133, v184, v183
	v_div_fmas_f32 v133, v133, v182, v184
	v_div_fixup_f32 v190, v133, v2, 1.0
	ds_read_b128 v[182:185], v1
	v_add_u32_e32 v133, s14, v1
	ds_read_b128 v[186:189], v133 offset:8192
	ds_read_b128 v[208:211], v133 offset:4096
	v_pk_mul_f32 v[216:217], v[190:191], v[216:217] op_sel_hi:[0,1]
	v_pk_mul_f32 v[196:197], v[190:191], v[196:197] op_sel_hi:[0,1]
	s_waitcnt lgkmcnt(2)
	v_pk_mul_f32 v[196:197], v[182:183], v[196:197]
	v_pk_mul_f32 v[182:183], v[184:185], v[216:217]
	s_waitcnt lgkmcnt(1)
	v_pk_add_f32 v[184:185], v[188:189], 1.0 op_sel_hi:[1,0]
	v_pk_add_f32 v[186:187], v[186:187], 1.0 op_sel_hi:[1,0]
	s_waitcnt lgkmcnt(0)
	v_pk_fma_f32 v[182:183], v[184:185], v[182:183], v[210:211]
	v_pk_fma_f32 v[184:185], v[186:187], v[196:197], v[208:209]
	v_lshl_add_u64 v[196:197], v[136:137], 0, s[12:13]
	s_and_b64 vcc, exec, s[4:5]
	v_cvt_pk_bf16_f32 v186, v184, v185
	v_cvt_pk_bf16_f32 v187, v182, v183
	global_store_dwordx2 v[196:197], v[186:187], off
	s_cbranch_vccnz .LBB0_1291
	v_pk_fma_f32 v[188:189], v[184:185], v[18:19], 0 op_sel_hi:[0,1,0]
	v_pk_fma_f32 v[188:189], v[184:185], v[10:11], v[188:189] op_sel:[1,0,0]
	v_pk_fma_f32 v[186:187], v[184:185], v[16:17], 0 op_sel_hi:[0,1,0]
	v_pk_fma_f32 v[208:209], v[182:183], v[34:35], v[188:189] op_sel_hi:[0,1,1]
	v_pk_fma_f32 v[188:189], v[184:185], v[12:13], 0 op_sel_hi:[0,1,0]
	v_pk_fma_f32 v[188:189], v[184:185], v[4:5], v[188:189] op_sel:[1,0,0]
	v_pk_fma_f32 v[186:187], v[184:185], v[8:9], v[186:187] op_sel:[1,0,0]
	v_pk_fma_f32 v[210:211], v[182:183], v[28:29], v[188:189] op_sel_hi:[0,1,1]
	v_pk_fma_f32 v[188:189], v[184:185], v[14:15], 0 op_sel_hi:[0,1,0]
	v_pk_fma_f32 v[184:185], v[184:185], v[6:7], v[188:189] op_sel:[1,0,0]
	v_pk_fma_f32 v[186:187], v[182:183], v[32:33], v[186:187] op_sel_hi:[0,1,1]
	v_pk_fma_f32 v[216:217], v[182:183], v[30:31], v[184:185] op_sel_hi:[0,1,1]
	v_mov_b32_e32 v2, v183
	v_pk_fma_f32 v[188:189], v[2:3], v[24:25], v[186:187] op_sel_hi:[0,1,1]
	v_pk_fma_f32 v[184:185], v[2:3], v[26:27], v[208:209] op_sel_hi:[0,1,1]
	v_pk_fma_f32 v[186:187], v[2:3], v[20:21], v[210:211] op_sel_hi:[0,1,1]
	v_pk_fma_f32 v[182:183], v[2:3], v[22:23], v[216:217] op_sel_hi:[0,1,1]
	s_branch .LBB0_1292

.LBB0_1296:
	ds_read_b128 v[192:195], v133 offset:11264
	ds_read_b128 v[198:201], v1 offset:3072
	ds_read_b128 v[208:211], v133 offset:7168
	v_mov_b32_e32 v216, v190
	v_mov_b32_e32 v217, v190
	v_pk_mul_f32 v[180:181], v[216:217], v[180:181]
	v_pk_mul_f32 v[178:179], v[190:191], v[178:179]
	s_waitcnt lgkmcnt(1)
	v_pk_mul_f32 v[180:181], v[200:201], v[180:181]
	v_pk_mul_f32 v[190:191], v[198:199], v[178:179]
	v_pk_add_f32 v[178:179], v[194:195], 1.0 op_sel_hi:[1,0]
	v_pk_add_f32 v[192:193], v[192:193], 1.0 op_sel_hi:[1,0]
	s_waitcnt lgkmcnt(0)
	v_pk_fma_f32 v[178:179], v[178:179], v[180:181], v[210:211]
	v_pk_fma_f32 v[180:181], v[192:193], v[190:191], v[208:209]
	s_and_b64 vcc, exec, s[4:5]
	v_cvt_pk_bf16_f32 v190, v180, v181
	v_cvt_pk_bf16_f32 v191, v178, v179
	global_store_dwordx2 v[196:197], v[190:191], off offset:1536
	s_cbranch_vccnz .LBB0_1304
	v_fma_f32 v2, v180, v128, v188
	v_fmac_f32_e32 v189, v180, v129
	v_fma_f32 v133, v180, v130, v184
	v_fmac_f32_e32 v185, v180, v131
	v_fma_f32 v184, v180, v88, v186
	v_fmac_f32_e32 v187, v180, v89
	v_fma_f32 v182, v180, v90, v182
	v_fmac_f32_e32 v183, v180, v91
	v_fmac_f32_e32 v2, v181, v96
	v_fmac_f32_e32 v189, v181, v97
	v_fmac_f32_e32 v133, v181, v98
	v_fmac_f32_e32 v185, v181, v99
	v_fmac_f32_e32 v184, v181, v112
	v_fmac_f32_e32 v187, v181, v113
	v_fmac_f32_e32 v182, v181, v114
	v_fmac_f32_e32 v183, v181, v115
	v_fmac_f32_e32 v2, v178, v116
	v_fmac_f32_e32 v189, v178, v117
	v_fmac_f32_e32 v133, v178, v118
	v_fmac_f32_e32 v185, v178, v119
	v_fmac_f32_e32 v184, v178, v120
	v_fmac_f32_e32 v187, v178, v121
	v_fmac_f32_e32 v182, v178, v122
	v_fmac_f32_e32 v183, v178, v123
	v_fmac_f32_e32 v2, v179, v124
	v_fmac_f32_e32 v189, v179, v125
	v_fmac_f32_e32 v133, v179, v126
	v_fmac_f32_e32 v185, v179, v127
	v_fmac_f32_e32 v184, v179, v100
	v_fmac_f32_e32 v187, v179, v101
	v_fmac_f32_e32 v182, v179, v102
	v_fmac_f32_e32 v183, v179, v103
	v_permlane32_swap_b32_e32 v2, v184
	v_permlane32_swap_b32_e32 v189, v187
	v_permlane32_swap_b32_e32 v133, v182
	v_permlane32_swap_b32_e32 v185, v183
	v_add_f32_e32 v2, v2, v184
	v_add_f32_e32 v178, v189, v187
	v_add_f32_e32 v133, v133, v182
	v_add_f32_e32 v179, v185, v183
	v_cndmask_b32_e64 v180, v2, v133, s[6:7]
	v_cndmask_b32_e64 v181, v178, v179, s[6:7]
	ds_swizzle_b32 v180, v180 offset:swizzle(SWAP,16)
	ds_swizzle_b32 v181, v181 offset:swizzle(SWAP,16)
	v_cndmask_b32_e64 v2, v133, v2, s[6:7]
	v_cndmask_b32_e64 v133, v179, v178, s[6:7]
	s_waitcnt lgkmcnt(1)
	v_add_f32_e32 v2, v2, v180
	s_waitcnt lgkmcnt(0)
	v_add_f32_e32 v133, v133, v181
	v_cndmask_b32_e64 v178, v2, v133, s[8:9]
	ds_swizzle_b32 v178, v178 offset:swizzle(SWAP,8)
	v_cndmask_b32_e64 v2, v133, v2, s[8:9]
	s_waitcnt lgkmcnt(0)
	v_add_f32_e32 v2, v2, v178
	ds_swizzle_b32 v133, v2 offset:swizzle(SWAP,4)
	s_waitcnt lgkmcnt(0)
	v_add_f32_e32 v2, v2, v133
	ds_swizzle_b32 v133, v2 offset:swizzle(SWAP,2)
	s_waitcnt lgkmcnt(0)
	v_add_f32_e32 v2, v2, v133
	s_waitcnt lgkmcnt(0)
	s_nop 1
	v_add_f32_dpp v2, v2, v2 quad_perm:[1,0,3,2] row_mask:0xf bank_mask:0xf
	s_nop 0
	v_readlane_b32 s67, v2, 0
	v_readlane_b32 s66, v2, 8
	v_readlane_b32 s63, v2, 16
	v_readlane_b32 s62, v2, 24
	v_readlane_b32 s27, v2, 32
	v_readlane_b32 s26, v2, 40
	v_readlane_b32 s61, v2, 48
	v_readlane_b32 s55, v2, 56
	s_and_saveexec_b64 s[42:43], s[10:11]
	s_cbranch_execz .LBB0_1303
	v_mov_b32_e32 v2, s67
	v_cmp_gt_f32_e64 s[12:13], s66, v2
	v_mov_b32_e32 v133, s66
	s_nop 0
	v_cndmask_b32_e64 v2, v2, v133, s[12:13]
	v_cmp_gt_f32_e64 s[14:15], s63, v2
	v_mov_b32_e32 v133, s63
	s_nop 0
	v_cndmask_b32_e64 v2, v2, v133, s[14:15]
	v_cmp_gt_f32_e64 s[16:17], s62, v2
	v_mov_b32_e32 v133, s62
	s_nop 0
	v_cndmask_b32_e64 v2, v2, v133, s[16:17]
	v_cmp_gt_f32_e64 s[18:19], s27, v2
	v_mov_b32_e32 v133, s27
	s_nop 0
	v_cndmask_b32_e64 v2, v2, v133, s[18:19]
	v_cmp_gt_f32_e64 s[22:23], s26, v2
	v_mov_b32_e32 v133, s26
	s_nop 0
	v_cndmask_b32_e64 v2, v2, v133, s[22:23]
	v_cmp_gt_f32_e64 s[24:25], s61, v2
	v_mov_b32_e32 v133, s61
	s_nop 0
	v_cndmask_b32_e64 v2, v2, v133, s[24:25]
	v_cndmask_b32_e64 v133, 0, 1, s[12:13]
	s_and_b64 s[12:13], s[14:15], exec
	v_readfirstlane_b32 s12, v133
	s_cselect_b32 s14, 2, s12
	s_and_b64 s[12:13], s[16:17], exec
	s_cselect_b32 s14, 3, s14
	s_and_b64 s[12:13], s[18:19], exec
	s_cselect_b32 s14, 4, s14
	s_and_b64 s[12:13], s[22:23], exec
	v_cmp_ngt_f32_e32 vcc, s55, v2
	s_cselect_b32 s14, 5, s14
	s_and_b64 s[12:13], s[24:25], exec
	s_cselect_b32 s14, 6, s14
	s_and_b64 s[12:13], vcc, exec
	s_cselect_b32 s60, s14, 7
	s_mov_b64 s[14:15], exec
	v_mbcnt_lo_u32_b32 v133, s14, 0
	v_mbcnt_hi_u32_b32 v133, s15, v133
	v_cmp_eq_u32_e64 s[12:13], 0, v133
	s_and_saveexec_b64 s[16:17], s[12:13]
	s_cbranch_execz .LBB0_1300
	s_lshl_b32 s12, s60, 2
	s_add_i32 s12, s12, 0
	s_add_i32 s12, s12, 0x20040
	s_bcnt1_i32_b64 s13, s[14:15]
	v_mov_b32_e32 v178, s12
	v_mov_b32_e32 v179, s13
	ds_add_rtn_u32 v179, v178, v179

.LBB0_1306:
	s_add_i32 s34, s52, s21
	s_cmp_gt_i32 s34, 0x83ff
	s_movk_i32 s17, 0x4f
	s_cbranch_scc1 .LBB0_1324
	s_mul_hi_i32 s12, s34, 0x3e0f83e1
	s_lshr_b32 s13, s12, 31
	s_ashr_i32 s16, s12, 11
	s_add_i32 s16, s16, s13
	s_mul_i32 s12, s16, 0xffffdf00
	s_add_i32 s12, s34, s12
	s_cmpk_lt_i32 s12, 0x100
	s_cselect_b64 s[14:15], -1, 0
	s_and_b64 s[12:13], s[64:65], s[14:15]
	s_movk_i32 s17, 0x51
	s_and_b64 vcc, exec, s[12:13]
	s_cbranch_vccnz .LBB0_1324
	s_waitcnt vmcnt(16)
	v_and_b32_e32 v189, 0xffff0000, v176
	v_and_b32_e32 v199, 0xffff0000, v177
	v_lshlrev_b32_e32 v188, 16, v176
	v_lshlrev_b32_e32 v198, 16, v177
	v_mul_f32_e32 v2, v189, v189
	v_mul_f32_e32 v133, v199, v199
	v_fmac_f32_e32 v2, v188, v188
	v_fmac_f32_e32 v133, v198, v198
	v_and_b32_e32 v191, 0xffff0000, v174
	v_and_b32_e32 v193, 0xffff0000, v175
	v_add_f32_e32 v2, v2, v133
	v_lshlrev_b32_e32 v190, 16, v174
	v_lshlrev_b32_e32 v192, 16, v175
	v_mul_f32_e32 v133, v191, v191
	v_mul_f32_e32 v174, v193, v193
	v_fmac_f32_e32 v133, v190, v190
	v_fmac_f32_e32 v174, v192, v192
	v_add_f32_e32 v133, v133, v174
	s_waitcnt vmcnt(12)
	v_and_b32_e32 v185, 0xffff0000, v172
	v_and_b32_e32 v187, 0xffff0000, v173
	v_add_f32_e32 v2, v2, v133
	v_lshlrev_b32_e32 v184, 16, v172
	v_lshlrev_b32_e32 v186, 16, v173
	v_mul_f32_e32 v133, v185, v185
	v_mul_f32_e32 v172, v187, v187
	v_fmac_f32_e32 v133, v184, v184
	v_fmac_f32_e32 v172, v186, v186
	v_add_f32_e32 v133, v133, v172
	v_lshlrev_b32_e32 v172, 16, v170
	v_and_b32_e32 v173, 0xffff0000, v170
	v_lshlrev_b32_e32 v170, 16, v171
	v_and_b32_e32 v171, 0xffff0000, v171
	v_add_f32_e32 v2, v2, v133
	v_mul_f32_e32 v133, v173, v173
	v_mul_f32_e32 v174, v171, v171
	v_fmac_f32_e32 v133, v172, v172
	v_fmac_f32_e32 v174, v170, v170
	v_add_f32_e32 v133, v133, v174
	v_add_f32_e32 v2, v2, v133
	s_lshl_b32 s16, s16, 13
	s_waitcnt lgkmcnt(0)
	s_nop 1
	v_add_f32_dpp v2, v2, v2 quad_perm:[1,0,3,2] row_mask:0xf bank_mask:0xf
	s_waitcnt lgkmcnt(0)
	s_nop 1
	v_add_f32_dpp v2, v2, v2 quad_perm:[2,3,0,1] row_mask:0xf bank_mask:0xf
	s_waitcnt lgkmcnt(0)
	s_nop 1
	v_add_f32_dpp v2, v2, v2 row_half_mirror row_mask:0xf bank_mask:0xf
	s_waitcnt lgkmcnt(0)
	s_nop 1
	v_add_f32_dpp v2, v2, v2 row_mirror row_mask:0xf bank_mask:0xf
	ds_swizzle_b32 v133, v2 offset:swizzle(SWAP,16)
	s_waitcnt lgkmcnt(0)
	v_add_f32_e32 v2, v2, v133
	v_mov_b32_e32 v133, v2
	s_nop 1
	v_permlane32_swap_b32_e32 v2, v133
	v_add_f32_e32 v2, v2, v133
	v_fmamk_f32 v2, v2, 0x3a800000, v213
	v_mul_f32_e32 v133, 0x4f800000, v2
	v_cmp_gt_f32_e32 vcc, s3, v2
	s_nop 1
	v_cndmask_b32_e32 v2, v2, v133, vcc
	v_sqrt_f32_e32 v133, v2
	s_nop 0
	v_add_u32_e32 v174, -1, v133
	v_fma_f32 v175, -v174, v133, v2
	v_cmp_ge_f32_e64 s[12:13], 0, v175
	v_add_u32_e32 v175, 1, v133
	s_nop 0
	v_cndmask_b32_e64 v174, v133, v174, s[12:13]
	v_fma_f32 v133, -v175, v133, v2
	v_cmp_lt_f32_e64 s[12:13], 0, v133
	s_nop 1
	v_cndmask_b32_e64 v133, v174, v175, s[12:13]
	v_mul_f32_e32 v174, 0x37800000, v133
	v_cndmask_b32_e32 v133, v133, v174, vcc
	v_cmp_class_f32_e32 vcc, v2, v215
	s_and_b64 s[12:13], s[14:15], exec
	s_cselect_b32 s14, 0x8000, s16
	v_cndmask_b32_e32 v2, v133, v2, vcc
	v_div_scale_f32 v133, s[12:13], v2, v2, 1.0
	v_rcp_f32_e32 v174, v133
	s_ashr_i32 s35, s34, 31
	s_lshl_b64 s[12:13], s[34:35], 11
	v_fma_f32 v175, -v133, v174, 1.0
	v_fmac_f32_e32 v174, v175, v174
	v_div_scale_f32 v175, vcc, 1.0, v2, 1.0
	v_mul_f32_e32 v176, v175, v174
	v_fma_f32 v177, -v133, v176, v175
	v_fmac_f32_e32 v176, v177, v174
	v_fma_f32 v133, -v133, v176, v175
	v_div_fmas_f32 v133, v133, v174, v176
	v_div_fixup_f32 v182, v133, v2, 1.0
	ds_read_b128 v[174:177], v1
	v_add_u32_e32 v133, s14, v1
	ds_read_b128 v[178:181], v133 offset:8192
	ds_read_b128 v[194:197], v133 offset:4096
	v_pk_mul_f32 v[198:199], v[182:183], v[198:199] op_sel_hi:[0,1]
	v_pk_mul_f32 v[188:189], v[182:183], v[188:189] op_sel_hi:[0,1]
	s_waitcnt lgkmcnt(2)
	v_pk_mul_f32 v[188:189], v[174:175], v[188:189]
	v_pk_mul_f32 v[174:175], v[176:177], v[198:199]
	s_waitcnt lgkmcnt(1)
	v_pk_add_f32 v[176:177], v[180:181], 1.0 op_sel_hi:[1,0]
	v_pk_add_f32 v[178:179], v[178:179], 1.0 op_sel_hi:[1,0]
	s_waitcnt lgkmcnt(0)
	v_pk_fma_f32 v[174:175], v[176:177], v[174:175], v[196:197]
	v_pk_fma_f32 v[176:177], v[178:179], v[188:189], v[194:195]
	v_lshl_add_u64 v[188:189], v[136:137], 0, s[12:13]
	s_and_b64 vcc, exec, s[4:5]
	v_cvt_pk_bf16_f32 v178, v176, v177
	v_cvt_pk_bf16_f32 v179, v174, v175
	global_store_dwordx2 v[188:189], v[178:179], off
	s_cbranch_vccnz .LBB0_1310
	v_pk_fma_f32 v[180:181], v[176:177], v[18:19], 0 op_sel_hi:[0,1,0]
	v_pk_fma_f32 v[180:181], v[176:177], v[10:11], v[180:181] op_sel:[1,0,0]
	v_pk_fma_f32 v[178:179], v[176:177], v[16:17], 0 op_sel_hi:[0,1,0]
	v_pk_fma_f32 v[194:195], v[174:175], v[34:35], v[180:181] op_sel_hi:[0,1,1]
	v_pk_fma_f32 v[180:181], v[176:177], v[12:13], 0 op_sel_hi:[0,1,0]
	v_pk_fma_f32 v[180:181], v[176:177], v[4:5], v[180:181] op_sel:[1,0,0]
	v_pk_fma_f32 v[178:179], v[176:177], v[8:9], v[178:179] op_sel:[1,0,0]
	v_pk_fma_f32 v[196:197], v[174:175], v[28:29], v[180:181] op_sel_hi:[0,1,1]
	v_pk_fma_f32 v[180:181], v[176:177], v[14:15], 0 op_sel_hi:[0,1,0]
	v_pk_fma_f32 v[176:177], v[176:177], v[6:7], v[180:181] op_sel:[1,0,0]
	v_pk_fma_f32 v[178:179], v[174:175], v[32:33], v[178:179] op_sel_hi:[0,1,1]
	v_pk_fma_f32 v[198:199], v[174:175], v[30:31], v[176:177] op_sel_hi:[0,1,1]
	v_mov_b32_e32 v2, v175
	v_pk_fma_f32 v[180:181], v[2:3], v[24:25], v[178:179] op_sel_hi:[0,1,1]
	v_pk_fma_f32 v[176:177], v[2:3], v[26:27], v[194:195] op_sel_hi:[0,1,1]
	v_pk_fma_f32 v[178:179], v[2:3], v[20:21], v[196:197] op_sel_hi:[0,1,1]
	v_pk_fma_f32 v[174:175], v[2:3], v[22:23], v[198:199] op_sel_hi:[0,1,1]
	s_branch .LBB0_1311

.LBB0_1315:
	ds_read_b128 v[184:187], v133 offset:11264
	ds_read_b128 v[190:193], v1 offset:3072
	ds_read_b128 v[194:197], v133 offset:7168
	v_mov_b32_e32 v198, v182
	v_mov_b32_e32 v199, v182
	v_pk_mul_f32 v[170:171], v[198:199], v[170:171]
	v_pk_mul_f32 v[172:173], v[182:183], v[172:173]
	s_waitcnt lgkmcnt(1)
	v_pk_mul_f32 v[170:171], v[192:193], v[170:171]
	v_pk_mul_f32 v[172:173], v[190:191], v[172:173]
	v_pk_add_f32 v[182:183], v[186:187], 1.0 op_sel_hi:[1,0]
	v_pk_add_f32 v[184:185], v[184:185], 1.0 op_sel_hi:[1,0]
	s_waitcnt lgkmcnt(0)
	v_pk_fma_f32 v[170:171], v[182:183], v[170:171], v[196:197]
	v_pk_fma_f32 v[172:173], v[184:185], v[172:173], v[194:195]
	s_and_b64 vcc, exec, s[4:5]
	v_cvt_pk_bf16_f32 v182, v172, v173
	v_cvt_pk_bf16_f32 v183, v170, v171
	global_store_dwordx2 v[188:189], v[182:183], off offset:1536
	s_cbranch_vccnz .LBB0_1323
	v_fma_f32 v2, v172, v128, v180
	v_fmac_f32_e32 v181, v172, v129
	v_fma_f32 v133, v172, v130, v176
	v_fmac_f32_e32 v177, v172, v131
	v_fma_f32 v176, v172, v88, v178
	v_fmac_f32_e32 v179, v172, v89
	v_fma_f32 v174, v172, v90, v174
	v_fmac_f32_e32 v175, v172, v91
	v_fmac_f32_e32 v2, v173, v96
	v_fmac_f32_e32 v181, v173, v97
	v_fmac_f32_e32 v133, v173, v98
	v_fmac_f32_e32 v177, v173, v99
	v_fmac_f32_e32 v176, v173, v112
	v_fmac_f32_e32 v179, v173, v113
	v_fmac_f32_e32 v174, v173, v114
	v_fmac_f32_e32 v175, v173, v115
	v_fmac_f32_e32 v2, v170, v116
	v_fmac_f32_e32 v181, v170, v117
	v_fmac_f32_e32 v133, v170, v118
	v_fmac_f32_e32 v177, v170, v119
	v_fmac_f32_e32 v176, v170, v120
	v_fmac_f32_e32 v179, v170, v121
	v_fmac_f32_e32 v174, v170, v122
	v_fmac_f32_e32 v175, v170, v123
	v_fmac_f32_e32 v2, v171, v124
	v_fmac_f32_e32 v181, v171, v125
	v_fmac_f32_e32 v133, v171, v126
	v_fmac_f32_e32 v177, v171, v127
	v_fmac_f32_e32 v176, v171, v100
	v_fmac_f32_e32 v179, v171, v101
	v_fmac_f32_e32 v174, v171, v102
	v_fmac_f32_e32 v175, v171, v103
	v_permlane32_swap_b32_e32 v2, v176
	v_permlane32_swap_b32_e32 v181, v179
	v_permlane32_swap_b32_e32 v133, v174
	v_permlane32_swap_b32_e32 v177, v175
	v_add_f32_e32 v2, v2, v176
	v_add_f32_e32 v170, v181, v179
	v_add_f32_e32 v133, v133, v174
	v_add_f32_e32 v171, v177, v175
	v_cndmask_b32_e64 v172, v2, v133, s[6:7]
	v_cndmask_b32_e64 v173, v170, v171, s[6:7]
	ds_swizzle_b32 v172, v172 offset:swizzle(SWAP,16)
	ds_swizzle_b32 v173, v173 offset:swizzle(SWAP,16)
	v_cndmask_b32_e64 v2, v133, v2, s[6:7]
	v_cndmask_b32_e64 v133, v171, v170, s[6:7]
	s_waitcnt lgkmcnt(1)
	v_add_f32_e32 v2, v2, v172
	s_waitcnt lgkmcnt(0)
	v_add_f32_e32 v133, v133, v173
	v_cndmask_b32_e64 v170, v2, v133, s[8:9]
	ds_swizzle_b32 v170, v170 offset:swizzle(SWAP,8)
	v_cndmask_b32_e64 v2, v133, v2, s[8:9]
	s_waitcnt lgkmcnt(0)
	v_add_f32_e32 v2, v2, v170
	ds_swizzle_b32 v133, v2 offset:swizzle(SWAP,4)
	s_waitcnt lgkmcnt(0)
	v_add_f32_e32 v2, v2, v133
	ds_swizzle_b32 v133, v2 offset:swizzle(SWAP,2)
	s_waitcnt lgkmcnt(0)
	v_add_f32_e32 v2, v2, v133
	s_waitcnt lgkmcnt(0)
	s_nop 1
	v_add_f32_dpp v2, v2, v2 quad_perm:[1,0,3,2] row_mask:0xf bank_mask:0xf
	s_nop 0
	v_readlane_b32 s67, v2, 0
	v_readlane_b32 s66, v2, 8
	v_readlane_b32 s63, v2, 16
	v_readlane_b32 s62, v2, 24
	v_readlane_b32 s27, v2, 32
	v_readlane_b32 s26, v2, 40
	v_readlane_b32 s61, v2, 48
	v_readlane_b32 s55, v2, 56
	s_and_saveexec_b64 s[42:43], s[10:11]
	s_cbranch_execz .LBB0_1322
	v_mov_b32_e32 v2, s67
	v_cmp_gt_f32_e64 s[12:13], s66, v2
	v_mov_b32_e32 v133, s66
	s_nop 0
	v_cndmask_b32_e64 v2, v2, v133, s[12:13]
	v_cmp_gt_f32_e64 s[14:15], s63, v2
	v_mov_b32_e32 v133, s63
	s_nop 0
	v_cndmask_b32_e64 v2, v2, v133, s[14:15]
	v_cmp_gt_f32_e64 s[16:17], s62, v2
	v_mov_b32_e32 v133, s62
	s_nop 0
	v_cndmask_b32_e64 v2, v2, v133, s[16:17]
	v_cmp_gt_f32_e64 s[18:19], s27, v2
	v_mov_b32_e32 v133, s27
	s_nop 0
	v_cndmask_b32_e64 v2, v2, v133, s[18:19]
	v_cmp_gt_f32_e64 s[22:23], s26, v2
	v_mov_b32_e32 v133, s26
	s_nop 0
	v_cndmask_b32_e64 v2, v2, v133, s[22:23]
	v_cmp_gt_f32_e64 s[24:25], s61, v2
	v_mov_b32_e32 v133, s61
	s_nop 0
	v_cndmask_b32_e64 v2, v2, v133, s[24:25]
	v_cndmask_b32_e64 v133, 0, 1, s[12:13]
	s_and_b64 s[12:13], s[14:15], exec
	v_readfirstlane_b32 s12, v133
	s_cselect_b32 s14, 2, s12
	s_and_b64 s[12:13], s[16:17], exec
	s_cselect_b32 s14, 3, s14
	s_and_b64 s[12:13], s[18:19], exec
	s_cselect_b32 s14, 4, s14
	s_and_b64 s[12:13], s[22:23], exec
	v_cmp_ngt_f32_e32 vcc, s55, v2
	s_cselect_b32 s14, 5, s14
	s_and_b64 s[12:13], s[24:25], exec
	s_cselect_b32 s14, 6, s14
	s_and_b64 s[12:13], vcc, exec
	s_cselect_b32 s60, s14, 7
	s_mov_b64 s[14:15], exec
	v_mbcnt_lo_u32_b32 v133, s14, 0
	v_mbcnt_hi_u32_b32 v133, s15, v133
	v_cmp_eq_u32_e64 s[12:13], 0, v133
	s_and_saveexec_b64 s[16:17], s[12:13]
	s_cbranch_execz .LBB0_1319
	s_lshl_b32 s12, s60, 2
	s_add_i32 s12, s12, 0
	s_add_i32 s12, s12, 0x20040
	s_bcnt1_i32_b64 s13, s[14:15]
	v_mov_b32_e32 v170, s12
	v_mov_b32_e32 v171, s13
	ds_add_rtn_u32 v171, v170, v171

.LBB0_1326:
	s_andn2_b64 vcc, exec, s[12:13]
	s_cbranch_vccnz .LBB0_1285
	s_add_i32 s34, s53, s21
	s_cmp_gt_i32 s34, 0x83ff
	s_cbranch_scc1 .LBB0_1285
	s_mul_hi_i32 s12, s34, 0x3e0f83e1
	s_lshr_b32 s13, s12, 31
	s_ashr_i32 s16, s12, 11
	s_add_i32 s16, s16, s13
	s_mul_i32 s12, s16, 0xffffdf00
	s_add_i32 s12, s34, s12
	s_cmpk_lt_i32 s12, 0x100
	s_cselect_b64 s[14:15], -1, 0
	s_and_b64 s[12:13], s[64:65], s[14:15]
	s_and_b64 vcc, exec, s[12:13]
	s_cbranch_vccnz .LBB0_1285
	s_waitcnt vmcnt(15)
	v_and_b32_e32 v181, 0xffff0000, v168
	v_and_b32_e32 v191, 0xffff0000, v169
	v_lshlrev_b32_e32 v180, 16, v168
	v_lshlrev_b32_e32 v190, 16, v169
	v_mul_f32_e32 v2, v181, v181
	v_mul_f32_e32 v133, v191, v191
	v_fmac_f32_e32 v2, v180, v180
	v_fmac_f32_e32 v133, v190, v190
	s_waitcnt vmcnt(13)
	v_and_b32_e32 v183, 0xffff0000, v166
	s_waitcnt vmcnt(12)
	v_and_b32_e32 v185, 0xffff0000, v167
	v_add_f32_e32 v2, v2, v133
	v_lshlrev_b32_e32 v182, 16, v166
	v_lshlrev_b32_e32 v184, 16, v167
	v_mul_f32_e32 v133, v183, v183
	v_mul_f32_e32 v166, v185, v185
	v_fmac_f32_e32 v133, v182, v182
	v_fmac_f32_e32 v166, v184, v184
	v_add_f32_e32 v133, v133, v166
	v_and_b32_e32 v177, 0xffff0000, v164
	v_and_b32_e32 v179, 0xffff0000, v165
	v_add_f32_e32 v2, v2, v133
	v_lshlrev_b32_e32 v176, 16, v164
	v_lshlrev_b32_e32 v178, 16, v165
	v_mul_f32_e32 v133, v177, v177
	v_mul_f32_e32 v164, v179, v179
	v_fmac_f32_e32 v133, v176, v176
	v_fmac_f32_e32 v164, v178, v178
	v_add_f32_e32 v133, v133, v164
	v_lshlrev_b32_e32 v164, 16, v162
	v_and_b32_e32 v165, 0xffff0000, v162
	v_lshlrev_b32_e32 v162, 16, v163
	v_and_b32_e32 v163, 0xffff0000, v163
	v_add_f32_e32 v2, v2, v133
	v_mul_f32_e32 v133, v165, v165
	v_mul_f32_e32 v166, v163, v163
	v_fmac_f32_e32 v133, v164, v164
	v_fmac_f32_e32 v166, v162, v162
	v_add_f32_e32 v133, v133, v166
	v_add_f32_e32 v2, v2, v133
	s_lshl_b32 s16, s16, 13
	s_waitcnt lgkmcnt(0)
	s_nop 1
	v_add_f32_dpp v2, v2, v2 quad_perm:[1,0,3,2] row_mask:0xf bank_mask:0xf
	s_waitcnt lgkmcnt(0)
	s_nop 1
	v_add_f32_dpp v2, v2, v2 quad_perm:[2,3,0,1] row_mask:0xf bank_mask:0xf
	s_waitcnt lgkmcnt(0)
	s_nop 1
	v_add_f32_dpp v2, v2, v2 row_half_mirror row_mask:0xf bank_mask:0xf
	s_waitcnt lgkmcnt(0)
	s_nop 1
	v_add_f32_dpp v2, v2, v2 row_mirror row_mask:0xf bank_mask:0xf
	ds_swizzle_b32 v133, v2 offset:swizzle(SWAP,16)
	s_waitcnt lgkmcnt(0)
	v_add_f32_e32 v2, v2, v133
	v_mov_b32_e32 v133, v2
	s_nop 1
	v_permlane32_swap_b32_e32 v2, v133
	v_add_f32_e32 v2, v2, v133
	v_fmamk_f32 v2, v2, 0x3a800000, v213
	v_mul_f32_e32 v133, 0x4f800000, v2
	v_cmp_gt_f32_e32 vcc, s3, v2
	s_nop 1
	v_cndmask_b32_e32 v2, v2, v133, vcc
	v_sqrt_f32_e32 v133, v2
	s_nop 0
	v_add_u32_e32 v166, -1, v133
	v_fma_f32 v167, -v166, v133, v2
	v_cmp_ge_f32_e64 s[12:13], 0, v167
	v_add_u32_e32 v167, 1, v133
	s_nop 0
	v_cndmask_b32_e64 v166, v133, v166, s[12:13]
	v_fma_f32 v133, -v167, v133, v2
	v_cmp_lt_f32_e64 s[12:13], 0, v133
	s_nop 1
	v_cndmask_b32_e64 v133, v166, v167, s[12:13]
	v_mul_f32_e32 v166, 0x37800000, v133
	v_cndmask_b32_e32 v133, v133, v166, vcc
	v_cmp_class_f32_e32 vcc, v2, v215
	s_and_b64 s[12:13], s[14:15], exec
	s_cselect_b32 s14, 0x8000, s16
	v_cndmask_b32_e32 v2, v133, v2, vcc
	v_div_scale_f32 v133, s[12:13], v2, v2, 1.0
	v_rcp_f32_e32 v166, v133
	s_ashr_i32 s35, s34, 31
	s_lshl_b64 s[12:13], s[34:35], 11
	v_fma_f32 v167, -v133, v166, 1.0
	v_fmac_f32_e32 v166, v167, v166
	v_div_scale_f32 v167, vcc, 1.0, v2, 1.0
	v_mul_f32_e32 v168, v167, v166
	v_fma_f32 v169, -v133, v168, v167
	v_fmac_f32_e32 v168, v169, v166
	v_fma_f32 v133, -v133, v168, v167
	v_div_fmas_f32 v133, v133, v166, v168
	v_div_fixup_f32 v174, v133, v2, 1.0
	ds_read_b128 v[166:169], v1
	v_add_u32_e32 v133, s14, v1
	ds_read_b128 v[170:173], v133 offset:8192
	ds_read_b128 v[186:189], v133 offset:4096
	v_pk_mul_f32 v[190:191], v[174:175], v[190:191] op_sel_hi:[0,1]
	v_pk_mul_f32 v[180:181], v[174:175], v[180:181] op_sel_hi:[0,1]
	s_waitcnt lgkmcnt(2)
	v_pk_mul_f32 v[180:181], v[166:167], v[180:181]
	v_pk_mul_f32 v[166:167], v[168:169], v[190:191]
	s_waitcnt lgkmcnt(1)
	v_pk_add_f32 v[168:169], v[172:173], 1.0 op_sel_hi:[1,0]
	v_pk_add_f32 v[170:171], v[170:171], 1.0 op_sel_hi:[1,0]
	s_waitcnt lgkmcnt(0)
	v_pk_fma_f32 v[166:167], v[168:169], v[166:167], v[188:189]
	v_pk_fma_f32 v[168:169], v[170:171], v[180:181], v[186:187]
	v_lshl_add_u64 v[180:181], v[136:137], 0, s[12:13]
	s_and_b64 vcc, exec, s[4:5]
	v_cvt_pk_bf16_f32 v170, v168, v169
	v_cvt_pk_bf16_f32 v171, v166, v167
	global_store_dwordx2 v[180:181], v[170:171], off
	s_cbranch_vccnz .LBB0_1331
	v_pk_fma_f32 v[172:173], v[168:169], v[18:19], 0 op_sel_hi:[0,1,0]
	v_pk_fma_f32 v[172:173], v[168:169], v[10:11], v[172:173] op_sel:[1,0,0]
	v_pk_fma_f32 v[170:171], v[168:169], v[16:17], 0 op_sel_hi:[0,1,0]
	v_pk_fma_f32 v[186:187], v[166:167], v[34:35], v[172:173] op_sel_hi:[0,1,1]
	v_pk_fma_f32 v[172:173], v[168:169], v[12:13], 0 op_sel_hi:[0,1,0]
	v_pk_fma_f32 v[172:173], v[168:169], v[4:5], v[172:173] op_sel:[1,0,0]
	v_pk_fma_f32 v[170:171], v[168:169], v[8:9], v[170:171] op_sel:[1,0,0]
	v_pk_fma_f32 v[188:189], v[166:167], v[28:29], v[172:173] op_sel_hi:[0,1,1]
	v_pk_fma_f32 v[172:173], v[168:169], v[14:15], 0 op_sel_hi:[0,1,0]
	v_pk_fma_f32 v[168:169], v[168:169], v[6:7], v[172:173] op_sel:[1,0,0]
	v_pk_fma_f32 v[170:171], v[166:167], v[32:33], v[170:171] op_sel_hi:[0,1,1]
	v_pk_fma_f32 v[190:191], v[166:167], v[30:31], v[168:169] op_sel_hi:[0,1,1]
	v_mov_b32_e32 v2, v167
	v_pk_fma_f32 v[172:173], v[2:3], v[24:25], v[170:171] op_sel_hi:[0,1,1]
	v_pk_fma_f32 v[168:169], v[2:3], v[26:27], v[186:187] op_sel_hi:[0,1,1]
	v_pk_fma_f32 v[170:171], v[2:3], v[20:21], v[188:189] op_sel_hi:[0,1,1]
	v_pk_fma_f32 v[166:167], v[2:3], v[22:23], v[190:191] op_sel_hi:[0,1,1]
	s_branch .LBB0_1332

.LBB0_1336:
	ds_read_b128 v[176:179], v133 offset:11264
	ds_read_b128 v[182:185], v1 offset:3072
	ds_read_b128 v[186:189], v133 offset:7168
	v_mov_b32_e32 v190, v174
	v_mov_b32_e32 v191, v174
	v_pk_mul_f32 v[162:163], v[190:191], v[162:163]
	v_pk_mul_f32 v[164:165], v[174:175], v[164:165]
	s_waitcnt lgkmcnt(1)
	v_pk_mul_f32 v[162:163], v[184:185], v[162:163]
	v_pk_mul_f32 v[164:165], v[182:183], v[164:165]
	v_pk_add_f32 v[174:175], v[178:179], 1.0 op_sel_hi:[1,0]
	v_pk_add_f32 v[176:177], v[176:177], 1.0 op_sel_hi:[1,0]
	s_waitcnt lgkmcnt(0)
	v_pk_fma_f32 v[162:163], v[174:175], v[162:163], v[188:189]
	v_pk_fma_f32 v[164:165], v[176:177], v[164:165], v[186:187]
	s_and_b64 vcc, exec, s[4:5]
	v_cvt_pk_bf16_f32 v174, v164, v165
	v_cvt_pk_bf16_f32 v175, v162, v163
	global_store_dwordx2 v[180:181], v[174:175], off offset:1536
	s_cbranch_vccnz .LBB0_1285
	v_fma_f32 v2, v164, v128, v172
	v_fmac_f32_e32 v173, v164, v129
	v_fma_f32 v133, v164, v130, v168
	v_fmac_f32_e32 v169, v164, v131
	v_fma_f32 v168, v164, v88, v170
	v_fmac_f32_e32 v171, v164, v89
	v_fma_f32 v166, v164, v90, v166
	v_fmac_f32_e32 v167, v164, v91
	v_fmac_f32_e32 v2, v165, v96
	v_fmac_f32_e32 v173, v165, v97
	v_fmac_f32_e32 v133, v165, v98
	v_fmac_f32_e32 v169, v165, v99
	v_fmac_f32_e32 v168, v165, v112
	v_fmac_f32_e32 v171, v165, v113
	v_fmac_f32_e32 v166, v165, v114
	v_fmac_f32_e32 v167, v165, v115
	v_fmac_f32_e32 v2, v162, v116
	v_fmac_f32_e32 v173, v162, v117
	v_fmac_f32_e32 v133, v162, v118
	v_fmac_f32_e32 v169, v162, v119
	v_fmac_f32_e32 v168, v162, v120
	v_fmac_f32_e32 v171, v162, v121
	v_fmac_f32_e32 v166, v162, v122
	v_fmac_f32_e32 v167, v162, v123
	v_fmac_f32_e32 v2, v163, v124
	v_fmac_f32_e32 v173, v163, v125
	v_fmac_f32_e32 v133, v163, v126
	v_fmac_f32_e32 v169, v163, v127
	v_fmac_f32_e32 v168, v163, v100
	v_fmac_f32_e32 v171, v163, v101
	v_fmac_f32_e32 v166, v163, v102
	v_fmac_f32_e32 v167, v163, v103
	v_permlane32_swap_b32_e32 v2, v168
	v_permlane32_swap_b32_e32 v173, v171
	v_permlane32_swap_b32_e32 v133, v166
	v_permlane32_swap_b32_e32 v169, v167
	v_add_f32_e32 v2, v2, v168
	v_add_f32_e32 v162, v173, v171
	v_add_f32_e32 v133, v133, v166
	v_add_f32_e32 v163, v169, v167
	v_cndmask_b32_e64 v164, v2, v133, s[6:7]
	v_cndmask_b32_e64 v165, v162, v163, s[6:7]
	ds_swizzle_b32 v164, v164 offset:swizzle(SWAP,16)
	ds_swizzle_b32 v165, v165 offset:swizzle(SWAP,16)
	v_cndmask_b32_e64 v2, v133, v2, s[6:7]
	v_cndmask_b32_e64 v133, v163, v162, s[6:7]
	s_waitcnt lgkmcnt(1)
	v_add_f32_e32 v2, v2, v164
	s_waitcnt lgkmcnt(0)
	v_add_f32_e32 v133, v133, v165
	v_cndmask_b32_e64 v162, v2, v133, s[8:9]
	ds_swizzle_b32 v162, v162 offset:swizzle(SWAP,8)
	v_cndmask_b32_e64 v2, v133, v2, s[8:9]
	s_waitcnt lgkmcnt(0)
	v_add_f32_e32 v2, v2, v162
	ds_swizzle_b32 v133, v2 offset:swizzle(SWAP,4)
	s_waitcnt lgkmcnt(0)
	v_add_f32_e32 v2, v2, v133
	ds_swizzle_b32 v133, v2 offset:swizzle(SWAP,2)
	s_waitcnt lgkmcnt(0)
	v_add_f32_e32 v2, v2, v133
	s_waitcnt lgkmcnt(0)
	s_nop 1
	v_add_f32_dpp v2, v2, v2 quad_perm:[1,0,3,2] row_mask:0xf bank_mask:0xf
	s_nop 0
	v_readlane_b32 s67, v2, 0
	v_readlane_b32 s66, v2, 8
	v_readlane_b32 s63, v2, 16
	v_readlane_b32 s62, v2, 24
	v_readlane_b32 s27, v2, 32
	v_readlane_b32 s26, v2, 40
	v_readlane_b32 s61, v2, 48
	v_readlane_b32 s55, v2, 56
	s_and_saveexec_b64 s[42:43], s[10:11]
	s_cbranch_execz .LBB0_1284
	v_mov_b32_e32 v2, s67
	v_cmp_gt_f32_e64 s[12:13], s66, v2
	v_mov_b32_e32 v133, s66
	s_nop 0
	v_cndmask_b32_e64 v2, v2, v133, s[12:13]
	v_cmp_gt_f32_e64 s[14:15], s63, v2
	v_mov_b32_e32 v133, s63
	s_nop 0
	v_cndmask_b32_e64 v2, v2, v133, s[14:15]
	v_cmp_gt_f32_e64 s[16:17], s62, v2
	v_mov_b32_e32 v133, s62
	s_nop 0
	v_cndmask_b32_e64 v2, v2, v133, s[16:17]
	v_cmp_gt_f32_e64 s[18:19], s27, v2
	v_mov_b32_e32 v133, s27
	s_nop 0
	v_cndmask_b32_e64 v2, v2, v133, s[18:19]
	v_cmp_gt_f32_e64 s[22:23], s26, v2
	v_mov_b32_e32 v133, s26
	s_nop 0
	v_cndmask_b32_e64 v2, v2, v133, s[22:23]
	v_cmp_gt_f32_e64 s[24:25], s61, v2
	v_mov_b32_e32 v133, s61
	s_nop 0
	v_cndmask_b32_e64 v2, v2, v133, s[24:25]
	v_cndmask_b32_e64 v133, 0, 1, s[12:13]
	s_and_b64 s[12:13], s[14:15], exec
	v_readfirstlane_b32 s12, v133
	s_cselect_b32 s14, 2, s12
	s_and_b64 s[12:13], s[16:17], exec
	s_cselect_b32 s14, 3, s14
	s_and_b64 s[12:13], s[18:19], exec
	s_cselect_b32 s14, 4, s14
	s_and_b64 s[12:13], s[22:23], exec
	v_cmp_ngt_f32_e32 vcc, s55, v2
	s_cselect_b32 s14, 5, s14
	s_and_b64 s[12:13], s[24:25], exec
	s_cselect_b32 s14, 6, s14
	s_and_b64 s[12:13], vcc, exec
	s_cselect_b32 s60, s14, 7
	s_mov_b64 s[14:15], exec
	v_mbcnt_lo_u32_b32 v133, s14, 0
	v_mbcnt_hi_u32_b32 v133, s15, v133
	v_cmp_eq_u32_e64 s[12:13], 0, v133
	s_and_saveexec_b64 s[16:17], s[12:13]
	s_cbranch_execz .LBB0_1340
	s_lshl_b32 s12, s60, 2
	s_add_i32 s12, s12, 0
	s_add_i32 s12, s12, 0x20040
	s_bcnt1_i32_b64 s13, s[14:15]
	v_mov_b32_e32 v162, s12
	v_mov_b32_e32 v163, s13
	ds_add_rtn_u32 v163, v162, v163

.LBB0_1411:
	ds_swizzle_b32 v7, v6 offset:swizzle(SWAP,1)
	v_cmp_eq_u32_e64 s[6:7], 0, v1
	s_waitcnt lgkmcnt(0)
	s_nop 1
	v_add_f32_dpp v2, v2, v2 quad_perm:[1,0,3,2] row_mask:0xf bank_mask:0xf
	v_add_f32_e32 v5, v6, v7
	ds_swizzle_b32 v7, v5 offset:swizzle(SWAP,2)
	s_waitcnt lgkmcnt(0)
	s_nop 1
	v_add_f32_dpp v2, v2, v2 quad_perm:[2,3,0,1] row_mask:0xf bank_mask:0xf
	v_add_f32_e32 v5, v5, v7
	ds_swizzle_b32 v7, v5 offset:swizzle(SWAP,4)
	s_waitcnt lgkmcnt(0)
	s_nop 1
	v_add_f32_dpp v2, v2, v2 row_half_mirror row_mask:0xf bank_mask:0xf
	v_add_f32_e32 v5, v5, v7
	ds_swizzle_b32 v7, v5 offset:swizzle(SWAP,8)
	s_waitcnt lgkmcnt(0)
	s_nop 1
	v_add_f32_dpp v2, v2, v2 row_mirror row_mask:0xf bank_mask:0xf
	v_add_f32_e32 v6, v5, v7
	ds_swizzle_b32 v5, v2 offset:swizzle(SWAP,16)
	ds_swizzle_b32 v7, v6 offset:swizzle(SWAP,16)
	s_waitcnt lgkmcnt(0)
	v_add_f32_e32 v5, v2, v5
	v_add_f32_e32 v2, v6, v7
	v_mov_b32_e32 v6, v5
	v_mov_b32_e32 v7, v2
	s_nop 0
	v_permlane32_swap_b32_e32 v5, v6
	v_permlane32_swap_b32_e32 v2, v7
	s_and_saveexec_b64 s[8:9], s[6:7]
	s_cbranch_execz .LBB0_1413
	v_add_f32_e32 v5, v5, v6
	s_lshl_b32 s10, s20, 2
	v_cvt_i32_f32_e32 v5, v5
	v_add_f32_e32 v2, v2, v7
	s_add_i32 s10, s10, 0
	v_cvt_i32_f32_e32 v2, v2
	s_add_i32 s10, s10, 0x20000
	v_mov_b32_e32 v6, s10
	ds_write_b32 v6, v5 offset:96
	ds_write_b32 v6, v2 offset:128

.LBB0_1856:
	s_mul_hi_i32 s2, s4, 0x3e0f83e1
	s_lshr_b32 s3, s2, 31
	s_ashr_i32 s2, s2, 11
	s_add_i32 s14, s2, s3
	v_lshl_add_u32 v63, s14, 12, v60
	ds_read_b128 v[64:67], v63 offset:45056
	ds_read_b128 v[68:71], v63 offset:46080
	v_lshlrev_b32_e32 v76, 16, v48
	v_and_b32_e32 v77, 0xffff0000, v48
	v_lshlrev_b32_e32 v78, 16, v49
	v_and_b32_e32 v79, 0xffff0000, v49
	s_waitcnt vmcnt(7)
	v_lshlrev_b32_e32 v48, 16, v54
	s_waitcnt vmcnt(3)
	v_and_b32_e32 v49, 0xffff0000, v58
	v_lshlrev_b32_e32 v80, 16, v44
	v_and_b32_e32 v81, 0xffff0000, v44
	v_lshlrev_b32_e32 v82, 16, v45
	v_and_b32_e32 v83, 0xffff0000, v45
	v_lshlrev_b32_e32 v44, 16, v58
	v_and_b32_e32 v45, 0xffff0000, v54
	v_pk_mul_f32 v[48:49], v[32:33], v[48:49]
	v_lshlrev_b32_e32 v72, 16, v56
	v_and_b32_e32 v73, 0xffff0000, v56
	v_pk_fma_f32 v[44:45], v[32:33], v[44:45], v[48:49] op_sel:[1,0,0] op_sel_hi:[0,1,1]
	v_lshlrev_b32_e32 v48, 16, v55
	v_and_b32_e32 v49, 0xffff0000, v59
	s_waitcnt lgkmcnt(1)
	v_pk_fma_f32 v[64:65], v[64:65], v[44:45], v[72:73]
	v_lshlrev_b32_e32 v44, 16, v59
	v_and_b32_e32 v45, 0xffff0000, v55
	v_pk_mul_f32 v[48:49], v[32:33], v[48:49]
	v_lshlrev_b32_e32 v56, 16, v57
	v_and_b32_e32 v57, 0xffff0000, v57
	v_pk_fma_f32 v[44:45], v[32:33], v[44:45], v[48:49] op_sel:[1,0,0] op_sel_hi:[0,1,1]
	v_lshlrev_b32_e32 v48, 16, v46
	s_waitcnt vmcnt(2)
	v_and_b32_e32 v49, 0xffff0000, v50
	v_pk_fma_f32 v[54:55], v[66:67], v[44:45], v[56:57]
	v_lshlrev_b32_e32 v44, 16, v50
	v_and_b32_e32 v45, 0xffff0000, v46
	v_pk_mul_f32 v[48:49], v[32:33], v[48:49]
	v_lshlrev_b32_e32 v74, 16, v52
	v_and_b32_e32 v75, 0xffff0000, v52
	v_pk_fma_f32 v[44:45], v[32:33], v[44:45], v[48:49] op_sel:[1,0,0] op_sel_hi:[0,1,1]
	s_waitcnt lgkmcnt(0)
	v_pk_fma_f32 v[56:57], v[68:69], v[44:45], v[74:75]
	v_and_b32_e32 v45, 0xffff0000, v47
	v_lshlrev_b32_e32 v46, 16, v47
	v_and_b32_e32 v47, 0xffff0000, v51
	v_lshlrev_b32_e32 v44, 16, v51
	v_pk_mul_f32 v[46:47], v[32:33], v[46:47]
	v_lshlrev_b32_e32 v52, 16, v53
	v_and_b32_e32 v53, 0xffff0000, v53
	v_pk_fma_f32 v[44:45], v[32:33], v[44:45], v[46:47] op_sel:[1,0,0] op_sel_hi:[0,1,1]
	v_pk_fma_f32 v[52:53], v[70:71], v[44:45], v[52:53]
	ds_read_b128 v[44:47], v63 offset:47104
	v_lshlrev_b32_e32 v50, 16, v40
	s_waitcnt vmcnt(1)
	v_and_b32_e32 v51, 0xffff0000, v42
	v_lshlrev_b32_e32 v48, 16, v42
	v_and_b32_e32 v49, 0xffff0000, v40
	v_pk_mul_f32 v[50:51], v[32:33], v[50:51]
	v_lshlrev_b32_e32 v40, 16, v41
	v_pk_fma_f32 v[58:59], v[32:33], v[48:49], v[50:51] op_sel:[1,0,0] op_sel_hi:[0,1,1]
	ds_read_b128 v[48:51], v63 offset:48128
	s_waitcnt lgkmcnt(1)
	v_pk_fma_f32 v[44:45], v[44:45], v[58:59], v[76:77]
	v_and_b32_e32 v59, 0xffff0000, v41
	v_and_b32_e32 v41, 0xffff0000, v43
	v_lshlrev_b32_e32 v58, 16, v43
	v_pk_mul_f32 v[40:41], v[32:33], v[40:41]
	s_waitcnt vmcnt(0)
	v_lshlrev_b32_e32 v42, 16, v38
	v_pk_fma_f32 v[40:41], v[32:33], v[58:59], v[40:41] op_sel:[1,0,0] op_sel_hi:[0,1,1]
	v_pk_fma_f32 v[40:41], v[46:47], v[40:41], v[78:79]
	v_lshlrev_b32_e32 v46, 16, v36
	v_and_b32_e32 v47, 0xffff0000, v38
	v_and_b32_e32 v43, 0xffff0000, v36
	v_pk_mul_f32 v[46:47], v[32:33], v[46:47]
	v_lshlrev_b32_e32 v36, 16, v37
	v_pk_fma_f32 v[42:43], v[32:33], v[42:43], v[46:47] op_sel:[1,0,0] op_sel_hi:[0,1,1]
	v_and_b32_e32 v47, 0xffff0000, v37
	v_and_b32_e32 v37, 0xffff0000, v39
	v_lshlrev_b32_e32 v46, 16, v39
	v_pk_mul_f32 v[36:37], v[32:33], v[36:37]
	s_waitcnt lgkmcnt(0)
	v_pk_fma_f32 v[42:43], v[48:49], v[42:43], v[80:81]
	v_pk_fma_f32 v[32:33], v[32:33], v[46:47], v[36:37] op_sel:[1,0,0] op_sel_hi:[0,1,1]
	v_pk_mul_f32 v[36:37], v[64:65], v[64:65]
	v_pk_mul_f32 v[38:39], v[54:55], v[54:55]
	v_pk_mul_f32 v[46:47], v[56:57], v[56:57]
	v_pk_mul_f32 v[48:49], v[52:53], v[52:53]
	v_pk_fma_f32 v[32:33], v[50:51], v[32:33], v[82:83]
	v_pk_mul_f32 v[50:51], v[44:45], v[44:45]
	v_pk_mul_f32 v[58:59], v[40:41], v[40:41]
	v_add_f32_e32 v48, v48, v49
	v_add_f32_e32 v46, v46, v47
	v_add_f32_e32 v38, v38, v39
	v_add_f32_e32 v36, v36, v37
	v_add_f32_e32 v46, v46, v48
	v_add_f32_e32 v36, v36, v38
	v_add_f32_e32 v37, v58, v59
	v_add_f32_e32 v38, v50, v51
	v_pk_mul_f32 v[66:67], v[42:43], v[42:43]
	v_pk_mul_f32 v[68:69], v[32:33], v[32:33]
	v_add_f32_e32 v36, v36, v46
	v_add_f32_e32 v37, v38, v37
	v_add_f32_e32 v36, v36, v37
	v_add_f32_e32 v37, v68, v69
	v_add_f32_e32 v38, v66, v67
	v_add_f32_e32 v37, v38, v37
	v_add_f32_e32 v36, v36, v37
	s_ashr_i32 s15, s14, 31
	v_mov_b64_e32 v[48:49], v[28:29]
	s_waitcnt lgkmcnt(0)
	s_nop 1
	v_add_f32_dpp v36, v36, v36 quad_perm:[1,0,3,2] row_mask:0xf bank_mask:0xf
	s_waitcnt lgkmcnt(0)
	s_nop 1
	v_add_f32_dpp v36, v36, v36 quad_perm:[2,3,0,1] row_mask:0xf bank_mask:0xf
	s_waitcnt lgkmcnt(0)
	s_nop 1
	v_add_f32_dpp v36, v36, v36 row_half_mirror row_mask:0xf bank_mask:0xf
	s_waitcnt lgkmcnt(0)
	s_nop 1
	v_add_f32_dpp v36, v36, v36 row_mirror row_mask:0xf bank_mask:0xf
	ds_swizzle_b32 v37, v36 offset:swizzle(SWAP,16)
	s_waitcnt lgkmcnt(0)
	v_add_f32_e32 v36, v36, v37
	v_mov_b32_e32 v37, v36
	s_nop 1
	v_permlane32_swap_b32_e32 v36, v37
	v_add_f32_e32 v36, v36, v37
	v_fmamk_f32 v36, v36, 0x3a800000, v16
	v_mul_f32_e32 v37, 0x4f800000, v36
	v_cmp_gt_f32_e32 vcc, s19, v36
	s_nop 1
	v_cndmask_b32_e32 v36, v36, v37, vcc
	v_sqrt_f32_e32 v37, v36
	s_nop 0
	v_add_u32_e32 v38, -1, v37
	v_fma_f32 v39, -v38, v37, v36
	v_cmp_ge_f32_e64 s[2:3], 0, v39
	v_add_u32_e32 v39, 1, v37
	s_nop 0
	v_cndmask_b32_e64 v38, v37, v38, s[2:3]
	v_fma_f32 v37, -v39, v37, v36
	v_cmp_lt_f32_e64 s[2:3], 0, v37
	s_nop 1
	v_cndmask_b32_e64 v37, v38, v39, s[2:3]
	v_mul_f32_e32 v38, 0x37800000, v37
	v_cndmask_b32_e32 v37, v37, v38, vcc
	v_cmp_class_f32_e32 vcc, v36, v61
	s_nop 1
	v_cndmask_b32_e32 v36, v37, v36, vcc
	v_div_scale_f32 v37, s[2:3], v36, v36, 1.0
	v_rcp_f32_e32 v38, v37
	s_mul_i32 s2, s14, 0xffffdf00
	s_add_i32 s2, s4, s2
	s_addk_i32 s2, 0xff00
	v_fma_f32 v39, -v37, v38, 1.0
	v_fmac_f32_e32 v38, v39, v38
	v_div_scale_f32 v39, vcc, 1.0, v36, 1.0
	v_mul_f32_e32 v46, v39, v38
	v_fma_f32 v47, -v37, v46, v39
	v_fmac_f32_e32 v46, v47, v38
	v_fma_f32 v37, -v37, v46, v39
	s_ashr_i32 s3, s2, 31
	s_lshl_b64 s[14:15], s[14:15], 25
	v_div_fmas_f32 v37, v37, v38, v46
	s_add_u32 s4, s6, s14
	v_div_fixup_f32 v46, v37, v36, 1.0
	s_addc_u32 s11, s7, s15
	s_lshl_b64 s[2:3], s[2:3], 12
	s_add_u32 s2, s4, s2
	v_pk_mul_f32 v[36:37], v[46:47], v[64:65] op_sel_hi:[0,1]
	v_pk_mul_f32 v[38:39], v[46:47], v[54:55] op_sel_hi:[0,1]
	s_addc_u32 s3, s11, s3
	v_pk_mul_f32 v[38:39], v[38:39], v[2:3]
	v_pk_mul_f32 v[36:37], v[36:37], v[0:1]
	global_store_dwordx4 v62, v[36:39], s[2:3]
	v_pk_mul_f32 v[32:33], v[46:47], v[32:33] op_sel_hi:[0,1]
	s_andn2_b64 vcc, exec, s[12:13]
	v_pk_mul_f32 v[36:37], v[46:47], v[56:57] op_sel_hi:[0,1]
	v_pk_mul_f32 v[38:39], v[46:47], v[52:53] op_sel_hi:[0,1]
	v_pk_mul_f32 v[38:39], v[38:39], v[6:7]
	v_pk_mul_f32 v[36:37], v[36:37], v[4:5]
	global_store_dwordx4 v62, v[36:39], s[2:3] offset:1024
	v_mov_b64_e32 v[52:53], v[26:27]
	v_mov_b64_e32 v[56:57], v[24:25]
	v_pk_mul_f32 v[36:37], v[46:47], v[44:45] op_sel_hi:[0,1]
	v_pk_mul_f32 v[38:39], v[46:47], v[40:41] op_sel_hi:[0,1]
	v_pk_mul_f32 v[38:39], v[38:39], v[10:11]
	v_pk_mul_f32 v[36:37], v[36:37], v[8:9]
	global_store_dwordx4 v62, v[36:39], s[2:3] offset:2048
	v_mov_b64_e32 v[44:45], v[30:31]
	s_mov_b32 s4, s10
	v_pk_mul_f32 v[36:37], v[46:47], v[42:43] op_sel_hi:[0,1]
	v_pk_mul_f32 v[38:39], v[32:33], v[14:15]
	v_pk_mul_f32 v[36:37], v[36:37], v[12:13]
	v_mov_b64_e32 v[32:33], v[34:35]
	global_store_dwordx4 v62, v[36:39], s[2:3] offset:3072
	s_cbranch_vccz .LBB0_1862
